# scan_s3 main body by hand: dwordx4 row loads/stores + permlane16/32 swap 4x4 transposes (80 loads + 16 stores per item instead of 320 + 64)
# speedup vs baseline: 1.0035x; 1.0035x over previous
; __device__ __forceinline__ float bf_lo(unsigned w) { return __uint_as_float(w << 16); }
; __device__ __forceinline__ float bf_hi(unsigned w) { return __uint_as_float(w & 0xffff0000u); }
; __device__ __forceinline__ void scan_s3(CTXA) {
;     ...
;         const size_t e0 = ((size_t)b * S + chunk * 64) * D + ch;
;         const unsigned* la0 = (const unsigned*)(LA + e0); const unsigned* bb0 = (const unsigned*)(BB + e0);
;         const unsigned* la1 = (const unsigned*)(LA + (size_t)T * D + e0); const unsigned* bb1 = (const unsigned*)(BB + (size_t)T * D + e0);
;         const unsigned* gg = (const unsigned*)(GG + e0); unsigned* yy = (unsigned*)(Y + e0);
;         float fv0[64], fv1[64];
; #pragma unroll
;         for (int g = 0; g < 4; ++g) { unsigned wl[16], wb[16];
; #pragma unroll
;             for (int q = 0; q < 16; ++q) { const int t = g * 16 + q; wl[q] = __builtin_nontemporal_load(la0 + (size_t)t * (D / 2)); wb[q] = __builtin_nontemporal_load(bb0 + (size_t)t * (D / 2)); }
; #pragma unroll
;             for (int q = 0; q < 16; ++q) { const int t = g * 16 + q; hf0 = __expf(bf_lo(wl[q])) * hf0 + bf_lo(wb[q]); hf1 = __expf(bf_hi(wl[q])) * hf1 + bf_hi(wb[q]); fv0[t] = hf0; fv1[t] = hf1; } }
.LBB0_171:
	s_ashr_i32 s7, s1, 6
	s_lshl_b32 s1, s6, 3
	s_add_i32 s1, s1, s7
	s_cmpk_gt_i32 s1, 0x7ff
	s_cbranch_scc1 .LBB0_184
	v_readlane_b32 s12, v254, 51
	s_lshl_b32 s2, s34, 3
	s_ashr_i32 s10, s0, 31
	v_readlane_b32 s14, v254, 53
	v_readlane_b32 s15, v254, 54
	s_add_u32 s8, s14, s0
	s_addc_u32 s9, s15, s10
	s_add_u32 s70, s8, 0x2c400000
	s_addc_u32 s71, s9, 0
	s_add_u32 s72, s8, 0x30400000
	s_addc_u32 s73, s9, 0
	s_add_u32 s74, s8, 0x36400000
	s_addc_u32 s75, s9, 0
	s_add_u32 s76, s8, 0x36600000
	s_addc_u32 s77, s9, 0
	s_add_u32 s78, s8, 0x26400000
	s_addc_u32 s79, s9, 0
	s_add_u32 s80, s8, 0x34400000
	s_addc_u32 s81, s9, 0
	s_add_u32 s82, s8, 0x2e400000
	s_addc_u32 s83, s9, 0
	s_add_u32 s84, s8, 0x32400000
	s_addc_u32 s85, s9, 0
	v_readlane_b32 s8, v254, 48
	s_add_u32 s8, s8, s0
	v_readlane_b32 s9, v254, 49
	v_readlane_b32 s13, v254, 52
	s_addc_u32 s9, s9, s10
	s_lshl_b32 s6, s6, 10
	s_lshl_b32 s7, s7, 7
	s_add_i32 s12, s6, s7
	s_lshl_b32 s13, s34, 10
	v_readlane_b32 s6, v254, 50
	v_lshlrev_b32_e32 v1, 1, v1
	s_add_u32 s14, s6, s0
	v_readlane_b32 s0, v254, 55
	v_and_b32_e32 v16, 15, v238
	v_bfe_u32 v1, v238, 4, 2
	v_lshlrev_b32_e32 v16, 3, v16
	v_lshl_or_b32 v16, v1, 1, v16
	s_addc_u32 s15, s0, s10
	s_branch .LBB0_174
.LBB0_173:
	s_lshl_b32 s6, s10, 22
	s_lshl_b32 s0, s0, 16
	s_or_b32 s6, s6, s0
	v_bfe_u32 v1, v2, 1, 2
	v_and_b32_e32 v2, 0xfffffff9, v2
	v_or_b32_e32 v3, s6, v2
	v_lshlrev_b32_e32 v3, 1, v3
	v_lshl_add_u32 v3, v1, 11, v3
	v_add_u32_e32 v4, 0x1e000, v3
	v_add_u32_e32 v5, 0x1e000, v3
	global_load_dwordx4 v[198:201], v3, s[70:71] nt
	global_load_dwordx4 v[202:205], v3, s[72:73] nt
	v_add_u32_e32 v3, 0x2000, v3
	global_load_dwordx4 v[206:209], v3, s[70:71] nt
	global_load_dwordx4 v[210:213], v3, s[72:73] nt
	v_add_u32_e32 v3, 0x2000, v3
	global_load_dwordx4 v[214:217], v3, s[70:71] nt
	global_load_dwordx4 v[218:221], v3, s[72:73] nt
	v_add_u32_e32 v3, 0x2000, v3
	global_load_dwordx4 v[222:225], v3, s[70:71] nt
	global_load_dwordx4 v[226:229], v3, s[72:73] nt
	v_add_u32_e32 v3, 0x2000, v3
	global_load_dwordx4 v[18:21], v4, s[82:83] nt
	global_load_dwordx4 v[22:25], v4, s[84:85] nt
	global_load_dwordx4 v[26:29], v4, s[78:79] nt
	v_add_u32_e32 v4, 0xffffe000, v4
	global_load_dwordx4 v[30:33], v4, s[82:83] nt
	global_load_dwordx4 v[34:37], v4, s[84:85] nt
	global_load_dwordx4 v[38:41], v4, s[78:79] nt
	v_add_u32_e32 v4, 0xffffe000, v4
	global_load_dwordx4 v[42:45], v4, s[82:83] nt
	global_load_dwordx4 v[46:49], v4, s[84:85] nt
	global_load_dwordx4 v[50:53], v4, s[78:79] nt
	v_add_u32_e32 v4, 0xffffe000, v4
	global_load_dwordx4 v[54:57], v4, s[82:83] nt
	global_load_dwordx4 v[58:61], v4, s[84:85] nt
	global_load_dwordx4 v[62:65], v4, s[78:79] nt
	v_add_u32_e32 v4, 0xffffe000, v4
	s_waitcnt vmcnt(18)
	v_permlane16_swap_b32_e32 v198, v199
	v_permlane16_swap_b32_e32 v200, v201
	v_permlane16_swap_b32_e32 v202, v203
	v_permlane16_swap_b32_e32 v204, v205
	v_permlane32_swap_b32_e32 v198, v200
	v_permlane32_swap_b32_e32 v199, v201
	v_permlane32_swap_b32_e32 v202, v204
	v_permlane32_swap_b32_e32 v203, v205
	v_and_b32_e32 v6, 0xffff0000, v198
	v_lshlrev_b32_e32 v198, 16, v198
	v_and_b32_e32 v7, 0xffff0000, v199
	v_lshlrev_b32_e32 v199, 16, v199
	v_and_b32_e32 v14, 0xffff0000, v200
	v_lshlrev_b32_e32 v200, 16, v200
	v_and_b32_e32 v15, 0xffff0000, v201
	v_lshlrev_b32_e32 v201, 16, v201
	v_mul_f32_e32 v198, 0x3fb8aa3b, v198
	v_mul_f32_e32 v6, 0x3fb8aa3b, v6
	v_mul_f32_e32 v199, 0x3fb8aa3b, v199
	v_mul_f32_e32 v7, 0x3fb8aa3b, v7
	v_mul_f32_e32 v200, 0x3fb8aa3b, v200
	v_mul_f32_e32 v14, 0x3fb8aa3b, v14
	v_mul_f32_e32 v201, 0x3fb8aa3b, v201
	v_mul_f32_e32 v15, 0x3fb8aa3b, v15
	v_exp_f32_e32 v198, v198
	v_exp_f32_e32 v6, v6
	v_exp_f32_e32 v199, v199
	v_exp_f32_e32 v7, v7
	v_exp_f32_e32 v200, v200
	v_exp_f32_e32 v14, v14
	v_exp_f32_e32 v201, v201
	v_exp_f32_e32 v15, v15
	v_lshlrev_b32_e32 v68, 16, v202
	v_and_b32_e32 v69, 0xffff0000, v202
	v_fmac_f32_e32 v68, v8, v198
	v_fmac_f32_e32 v69, v9, v6
	v_lshlrev_b32_e32 v70, 16, v203
	v_and_b32_e32 v71, 0xffff0000, v203
	v_fmac_f32_e32 v70, v68, v199
	v_fmac_f32_e32 v71, v69, v7
	v_lshlrev_b32_e32 v72, 16, v204
	v_and_b32_e32 v73, 0xffff0000, v204
	v_fmac_f32_e32 v72, v70, v200
	v_fmac_f32_e32 v73, v71, v14
	v_lshlrev_b32_e32 v74, 16, v205
	v_and_b32_e32 v75, 0xffff0000, v205
	v_fmac_f32_e32 v74, v72, v201
	v_fmac_f32_e32 v75, v73, v15
	global_load_dwordx4 v[198:201], v3, s[70:71] nt
	global_load_dwordx4 v[202:205], v3, s[72:73] nt
	v_add_u32_e32 v3, 0x2000, v3
	s_waitcnt vmcnt(18)
	v_permlane16_swap_b32_e32 v206, v207
	v_permlane16_swap_b32_e32 v208, v209
	v_permlane16_swap_b32_e32 v210, v211
	v_permlane16_swap_b32_e32 v212, v213
	v_permlane32_swap_b32_e32 v206, v208
	v_permlane32_swap_b32_e32 v207, v209
	v_permlane32_swap_b32_e32 v210, v212
	v_permlane32_swap_b32_e32 v211, v213
	v_and_b32_e32 v6, 0xffff0000, v206
	v_lshlrev_b32_e32 v206, 16, v206
	v_and_b32_e32 v7, 0xffff0000, v207
	v_lshlrev_b32_e32 v207, 16, v207
	v_and_b32_e32 v14, 0xffff0000, v208
	v_lshlrev_b32_e32 v208, 16, v208
	v_and_b32_e32 v15, 0xffff0000, v209
	v_lshlrev_b32_e32 v209, 16, v209
	v_mul_f32_e32 v206, 0x3fb8aa3b, v206
	v_mul_f32_e32 v6, 0x3fb8aa3b, v6
	v_mul_f32_e32 v207, 0x3fb8aa3b, v207
	v_mul_f32_e32 v7, 0x3fb8aa3b, v7
	v_mul_f32_e32 v208, 0x3fb8aa3b, v208
	v_mul_f32_e32 v14, 0x3fb8aa3b, v14
	v_mul_f32_e32 v209, 0x3fb8aa3b, v209
	v_mul_f32_e32 v15, 0x3fb8aa3b, v15
	v_exp_f32_e32 v206, v206
	v_exp_f32_e32 v6, v6
	v_exp_f32_e32 v207, v207
	v_exp_f32_e32 v7, v7
	v_exp_f32_e32 v208, v208
	v_exp_f32_e32 v14, v14
	v_exp_f32_e32 v209, v209
	v_exp_f32_e32 v15, v15
	v_lshlrev_b32_e32 v76, 16, v210
	v_and_b32_e32 v77, 0xffff0000, v210
	v_fmac_f32_e32 v76, v74, v206
	v_fmac_f32_e32 v77, v75, v6
	v_lshlrev_b32_e32 v78, 16, v211
	v_and_b32_e32 v79, 0xffff0000, v211
	v_fmac_f32_e32 v78, v76, v207
	v_fmac_f32_e32 v79, v77, v7
	v_lshlrev_b32_e32 v80, 16, v212
	v_and_b32_e32 v81, 0xffff0000, v212
	v_fmac_f32_e32 v80, v78, v208
	v_fmac_f32_e32 v81, v79, v14
	v_lshlrev_b32_e32 v82, 16, v213
	v_and_b32_e32 v83, 0xffff0000, v213
	v_fmac_f32_e32 v82, v80, v209
	v_fmac_f32_e32 v83, v81, v15
	global_load_dwordx4 v[206:209], v3, s[70:71] nt
	global_load_dwordx4 v[210:213], v3, s[72:73] nt
	v_add_u32_e32 v3, 0x2000, v3
	s_waitcnt vmcnt(18)
; __device__ __forceinline__ float bf_lo(unsigned w) { return __uint_as_float(w << 16); }
; __device__ __forceinline__ float bf_hi(unsigned w) { return __uint_as_float(w & 0xffff0000u); }
; __device__ __forceinline__ void scan_s3(CTXA) {
;     ...
;         for (int g = 0; g < 4; ++g) { unsigned wl[16], wb[16];
; #pragma unroll
;             for (int q = 0; q < 16; ++q) { const int t = g * 16 + q; wl[q] = __builtin_nontemporal_load(la0 + (size_t)t * (D / 2)); wb[q] = __builtin_nontemporal_load(bb0 + (size_t)t * (D / 2)); }
; #pragma unroll
;             for (int q = 0; q < 16; ++q) { const int t = g * 16 + q; hf0 = __expf(bf_lo(wl[q])) * hf0 + bf_lo(wb[q]); hf1 = __expf(bf_hi(wl[q])) * hf1 + bf_hi(wb[q]); fv0[t] = hf0; fv1[t] = hf1; } }
	v_permlane16_swap_b32_e32 v214, v215
	v_permlane16_swap_b32_e32 v216, v217
	v_permlane16_swap_b32_e32 v218, v219
	v_permlane16_swap_b32_e32 v220, v221
	v_permlane32_swap_b32_e32 v214, v216
	v_permlane32_swap_b32_e32 v215, v217
	v_permlane32_swap_b32_e32 v218, v220
	v_permlane32_swap_b32_e32 v219, v221
	v_and_b32_e32 v6, 0xffff0000, v214
	v_lshlrev_b32_e32 v214, 16, v214
	v_and_b32_e32 v7, 0xffff0000, v215
	v_lshlrev_b32_e32 v215, 16, v215
	v_and_b32_e32 v14, 0xffff0000, v216
	v_lshlrev_b32_e32 v216, 16, v216
	v_and_b32_e32 v15, 0xffff0000, v217
	v_lshlrev_b32_e32 v217, 16, v217
	v_mul_f32_e32 v214, 0x3fb8aa3b, v214
	v_mul_f32_e32 v6, 0x3fb8aa3b, v6
	v_mul_f32_e32 v215, 0x3fb8aa3b, v215
	v_mul_f32_e32 v7, 0x3fb8aa3b, v7
	v_mul_f32_e32 v216, 0x3fb8aa3b, v216
	v_mul_f32_e32 v14, 0x3fb8aa3b, v14
	v_mul_f32_e32 v217, 0x3fb8aa3b, v217
	v_mul_f32_e32 v15, 0x3fb8aa3b, v15
	v_exp_f32_e32 v214, v214
	v_exp_f32_e32 v6, v6
	v_exp_f32_e32 v215, v215
	v_exp_f32_e32 v7, v7
	v_exp_f32_e32 v216, v216
	v_exp_f32_e32 v14, v14
	v_exp_f32_e32 v217, v217
	v_exp_f32_e32 v15, v15
	v_lshlrev_b32_e32 v84, 16, v218
	v_and_b32_e32 v85, 0xffff0000, v218
	v_fmac_f32_e32 v84, v82, v214
	v_fmac_f32_e32 v85, v83, v6
	v_lshlrev_b32_e32 v86, 16, v219
	v_and_b32_e32 v87, 0xffff0000, v219
	v_fmac_f32_e32 v86, v84, v215
	v_fmac_f32_e32 v87, v85, v7
	v_lshlrev_b32_e32 v88, 16, v220
	v_and_b32_e32 v89, 0xffff0000, v220
	v_fmac_f32_e32 v88, v86, v216
	v_fmac_f32_e32 v89, v87, v14
	v_lshlrev_b32_e32 v90, 16, v221
	v_and_b32_e32 v91, 0xffff0000, v221
	v_fmac_f32_e32 v90, v88, v217
	v_fmac_f32_e32 v91, v89, v15
	global_load_dwordx4 v[214:217], v3, s[70:71] nt
	global_load_dwordx4 v[218:221], v3, s[72:73] nt
	v_add_u32_e32 v3, 0x2000, v3
	s_waitcnt vmcnt(18)
	v_permlane16_swap_b32_e32 v222, v223
	v_permlane16_swap_b32_e32 v224, v225
	v_permlane16_swap_b32_e32 v226, v227
	v_permlane16_swap_b32_e32 v228, v229
	v_permlane32_swap_b32_e32 v222, v224
	v_permlane32_swap_b32_e32 v223, v225
	v_permlane32_swap_b32_e32 v226, v228
	v_permlane32_swap_b32_e32 v227, v229
	v_and_b32_e32 v6, 0xffff0000, v222
	v_lshlrev_b32_e32 v222, 16, v222
	v_and_b32_e32 v7, 0xffff0000, v223
	v_lshlrev_b32_e32 v223, 16, v223
	v_and_b32_e32 v14, 0xffff0000, v224
	v_lshlrev_b32_e32 v224, 16, v224
	v_and_b32_e32 v15, 0xffff0000, v225
	v_lshlrev_b32_e32 v225, 16, v225
	v_mul_f32_e32 v222, 0x3fb8aa3b, v222
	v_mul_f32_e32 v6, 0x3fb8aa3b, v6
	v_mul_f32_e32 v223, 0x3fb8aa3b, v223
	v_mul_f32_e32 v7, 0x3fb8aa3b, v7
	v_mul_f32_e32 v224, 0x3fb8aa3b, v224
	v_mul_f32_e32 v14, 0x3fb8aa3b, v14
	v_mul_f32_e32 v225, 0x3fb8aa3b, v225
	v_mul_f32_e32 v15, 0x3fb8aa3b, v15
	v_exp_f32_e32 v222, v222
	v_exp_f32_e32 v6, v6
	v_exp_f32_e32 v223, v223
	v_exp_f32_e32 v7, v7
	v_exp_f32_e32 v224, v224
	v_exp_f32_e32 v14, v14
	v_exp_f32_e32 v225, v225
	v_exp_f32_e32 v15, v15
	v_lshlrev_b32_e32 v92, 16, v226
	v_and_b32_e32 v93, 0xffff0000, v226
	v_fmac_f32_e32 v92, v90, v222
	v_fmac_f32_e32 v93, v91, v6
	v_lshlrev_b32_e32 v94, 16, v227
	v_and_b32_e32 v95, 0xffff0000, v227
	v_fmac_f32_e32 v94, v92, v223
	v_fmac_f32_e32 v95, v93, v7
	v_lshlrev_b32_e32 v96, 16, v228
	v_and_b32_e32 v97, 0xffff0000, v228
	v_fmac_f32_e32 v96, v94, v224
	v_fmac_f32_e32 v97, v95, v14
	v_lshlrev_b32_e32 v98, 16, v229
	v_and_b32_e32 v99, 0xffff0000, v229
	v_fmac_f32_e32 v98, v96, v225
	v_fmac_f32_e32 v99, v97, v15
	global_load_dwordx4 v[222:225], v3, s[70:71] nt
	global_load_dwordx4 v[226:229], v3, s[72:73] nt
	v_add_u32_e32 v3, 0x2000, v3
	s_waitcnt vmcnt(6)
	v_permlane16_swap_b32_e32 v198, v199
	v_permlane16_swap_b32_e32 v200, v201
	v_permlane16_swap_b32_e32 v202, v203
	v_permlane16_swap_b32_e32 v204, v205
	v_permlane32_swap_b32_e32 v198, v200
	v_permlane32_swap_b32_e32 v199, v201
	v_permlane32_swap_b32_e32 v202, v204
	v_permlane32_swap_b32_e32 v203, v205
	v_and_b32_e32 v6, 0xffff0000, v198
	v_lshlrev_b32_e32 v198, 16, v198
	v_and_b32_e32 v7, 0xffff0000, v199
	v_lshlrev_b32_e32 v199, 16, v199
	v_and_b32_e32 v14, 0xffff0000, v200
	v_lshlrev_b32_e32 v200, 16, v200
	v_and_b32_e32 v15, 0xffff0000, v201
	v_lshlrev_b32_e32 v201, 16, v201
	v_mul_f32_e32 v198, 0x3fb8aa3b, v198
	v_mul_f32_e32 v6, 0x3fb8aa3b, v6
	v_mul_f32_e32 v199, 0x3fb8aa3b, v199
	v_mul_f32_e32 v7, 0x3fb8aa3b, v7
	v_mul_f32_e32 v200, 0x3fb8aa3b, v200
	v_mul_f32_e32 v14, 0x3fb8aa3b, v14
	v_mul_f32_e32 v201, 0x3fb8aa3b, v201
	v_mul_f32_e32 v15, 0x3fb8aa3b, v15
	v_exp_f32_e32 v198, v198
	v_exp_f32_e32 v6, v6
	v_exp_f32_e32 v199, v199
	v_exp_f32_e32 v7, v7
	v_exp_f32_e32 v200, v200
	v_exp_f32_e32 v14, v14
	v_exp_f32_e32 v201, v201
	v_exp_f32_e32 v15, v15
	v_lshlrev_b32_e32 v100, 16, v202
	v_and_b32_e32 v101, 0xffff0000, v202
	v_fmac_f32_e32 v100, v98, v198
	v_fmac_f32_e32 v101, v99, v6
	v_lshlrev_b32_e32 v102, 16, v203
	v_and_b32_e32 v103, 0xffff0000, v203
	v_fmac_f32_e32 v102, v100, v199
	v_fmac_f32_e32 v103, v101, v7
	v_lshlrev_b32_e32 v104, 16, v204
	v_and_b32_e32 v105, 0xffff0000, v204
	v_fmac_f32_e32 v104, v102, v200
	v_fmac_f32_e32 v105, v103, v14
	v_lshlrev_b32_e32 v106, 16, v205
	v_and_b32_e32 v107, 0xffff0000, v205
	v_fmac_f32_e32 v106, v104, v201
	v_fmac_f32_e32 v107, v105, v15
	global_load_dwordx4 v[198:201], v3, s[70:71] nt
	global_load_dwordx4 v[202:205], v3, s[72:73] nt
	v_add_u32_e32 v3, 0x2000, v3
	s_waitcnt vmcnt(6)
; __device__ __forceinline__ float bf_lo(unsigned w) { return __uint_as_float(w << 16); }
; __device__ __forceinline__ float bf_hi(unsigned w) { return __uint_as_float(w & 0xffff0000u); }
; __device__ __forceinline__ void scan_s3(CTXA) {
;     ...
;         for (int g = 0; g < 4; ++g) { unsigned wl[16], wb[16];
; #pragma unroll
;             for (int q = 0; q < 16; ++q) { const int t = g * 16 + q; wl[q] = __builtin_nontemporal_load(la0 + (size_t)t * (D / 2)); wb[q] = __builtin_nontemporal_load(bb0 + (size_t)t * (D / 2)); }
; #pragma unroll
;             for (int q = 0; q < 16; ++q) { const int t = g * 16 + q; hf0 = __expf(bf_lo(wl[q])) * hf0 + bf_lo(wb[q]); hf1 = __expf(bf_hi(wl[q])) * hf1 + bf_hi(wb[q]); fv0[t] = hf0; fv1[t] = hf1; } }
	v_permlane16_swap_b32_e32 v206, v207
	v_permlane16_swap_b32_e32 v208, v209
	v_permlane16_swap_b32_e32 v210, v211
	v_permlane16_swap_b32_e32 v212, v213
	v_permlane32_swap_b32_e32 v206, v208
	v_permlane32_swap_b32_e32 v207, v209
	v_permlane32_swap_b32_e32 v210, v212
	v_permlane32_swap_b32_e32 v211, v213
	v_and_b32_e32 v6, 0xffff0000, v206
	v_lshlrev_b32_e32 v206, 16, v206
	v_and_b32_e32 v7, 0xffff0000, v207
	v_lshlrev_b32_e32 v207, 16, v207
	v_and_b32_e32 v14, 0xffff0000, v208
	v_lshlrev_b32_e32 v208, 16, v208
	v_and_b32_e32 v15, 0xffff0000, v209
	v_lshlrev_b32_e32 v209, 16, v209
	v_mul_f32_e32 v206, 0x3fb8aa3b, v206
	v_mul_f32_e32 v6, 0x3fb8aa3b, v6
	v_mul_f32_e32 v207, 0x3fb8aa3b, v207
	v_mul_f32_e32 v7, 0x3fb8aa3b, v7
	v_mul_f32_e32 v208, 0x3fb8aa3b, v208
	v_mul_f32_e32 v14, 0x3fb8aa3b, v14
	v_mul_f32_e32 v209, 0x3fb8aa3b, v209
	v_mul_f32_e32 v15, 0x3fb8aa3b, v15
	v_exp_f32_e32 v206, v206
	v_exp_f32_e32 v6, v6
	v_exp_f32_e32 v207, v207
	v_exp_f32_e32 v7, v7
	v_exp_f32_e32 v208, v208
	v_exp_f32_e32 v14, v14
	v_exp_f32_e32 v209, v209
	v_exp_f32_e32 v15, v15
	v_lshlrev_b32_e32 v108, 16, v210
	v_and_b32_e32 v109, 0xffff0000, v210
	v_fmac_f32_e32 v108, v106, v206
	v_fmac_f32_e32 v109, v107, v6
	v_lshlrev_b32_e32 v110, 16, v211
	v_and_b32_e32 v111, 0xffff0000, v211
	v_fmac_f32_e32 v110, v108, v207
	v_fmac_f32_e32 v111, v109, v7
	v_lshlrev_b32_e32 v112, 16, v212
	v_and_b32_e32 v113, 0xffff0000, v212
	v_fmac_f32_e32 v112, v110, v208
	v_fmac_f32_e32 v113, v111, v14
	v_lshlrev_b32_e32 v114, 16, v213
	v_and_b32_e32 v115, 0xffff0000, v213
	v_fmac_f32_e32 v114, v112, v209
	v_fmac_f32_e32 v115, v113, v15
	global_load_dwordx4 v[206:209], v3, s[70:71] nt
	global_load_dwordx4 v[210:213], v3, s[72:73] nt
	v_add_u32_e32 v3, 0x2000, v3
	s_waitcnt vmcnt(6)
	v_permlane16_swap_b32_e32 v214, v215
	v_permlane16_swap_b32_e32 v216, v217
	v_permlane16_swap_b32_e32 v218, v219
	v_permlane16_swap_b32_e32 v220, v221
	v_permlane32_swap_b32_e32 v214, v216
	v_permlane32_swap_b32_e32 v215, v217
	v_permlane32_swap_b32_e32 v218, v220
	v_permlane32_swap_b32_e32 v219, v221
	v_and_b32_e32 v6, 0xffff0000, v214
	v_lshlrev_b32_e32 v214, 16, v214
	v_and_b32_e32 v7, 0xffff0000, v215
	v_lshlrev_b32_e32 v215, 16, v215
	v_and_b32_e32 v14, 0xffff0000, v216
	v_lshlrev_b32_e32 v216, 16, v216
	v_and_b32_e32 v15, 0xffff0000, v217
	v_lshlrev_b32_e32 v217, 16, v217
	v_mul_f32_e32 v214, 0x3fb8aa3b, v214
	v_mul_f32_e32 v6, 0x3fb8aa3b, v6
	v_mul_f32_e32 v215, 0x3fb8aa3b, v215
	v_mul_f32_e32 v7, 0x3fb8aa3b, v7
	v_mul_f32_e32 v216, 0x3fb8aa3b, v216
	v_mul_f32_e32 v14, 0x3fb8aa3b, v14
	v_mul_f32_e32 v217, 0x3fb8aa3b, v217
	v_mul_f32_e32 v15, 0x3fb8aa3b, v15
	v_exp_f32_e32 v214, v214
	v_exp_f32_e32 v6, v6
	v_exp_f32_e32 v215, v215
	v_exp_f32_e32 v7, v7
	v_exp_f32_e32 v216, v216
	v_exp_f32_e32 v14, v14
	v_exp_f32_e32 v217, v217
	v_exp_f32_e32 v15, v15
	v_lshlrev_b32_e32 v116, 16, v218
	v_and_b32_e32 v117, 0xffff0000, v218
	v_fmac_f32_e32 v116, v114, v214
	v_fmac_f32_e32 v117, v115, v6
	v_lshlrev_b32_e32 v118, 16, v219
	v_and_b32_e32 v119, 0xffff0000, v219
	v_fmac_f32_e32 v118, v116, v215
	v_fmac_f32_e32 v119, v117, v7
	v_lshlrev_b32_e32 v120, 16, v220
	v_and_b32_e32 v121, 0xffff0000, v220
	v_fmac_f32_e32 v120, v118, v216
	v_fmac_f32_e32 v121, v119, v14
	v_lshlrev_b32_e32 v122, 16, v221
	v_and_b32_e32 v123, 0xffff0000, v221
	v_fmac_f32_e32 v122, v120, v217
	v_fmac_f32_e32 v123, v121, v15
	global_load_dwordx4 v[214:217], v3, s[70:71] nt
	global_load_dwordx4 v[218:221], v3, s[72:73] nt
	v_add_u32_e32 v3, 0x2000, v3
	s_waitcnt vmcnt(6)
	v_permlane16_swap_b32_e32 v222, v223
	v_permlane16_swap_b32_e32 v224, v225
	v_permlane16_swap_b32_e32 v226, v227
	v_permlane16_swap_b32_e32 v228, v229
	v_permlane32_swap_b32_e32 v222, v224
	v_permlane32_swap_b32_e32 v223, v225
	v_permlane32_swap_b32_e32 v226, v228
	v_permlane32_swap_b32_e32 v227, v229
	v_and_b32_e32 v6, 0xffff0000, v222
	v_lshlrev_b32_e32 v222, 16, v222
	v_and_b32_e32 v7, 0xffff0000, v223
	v_lshlrev_b32_e32 v223, 16, v223
	v_and_b32_e32 v14, 0xffff0000, v224
	v_lshlrev_b32_e32 v224, 16, v224
	v_and_b32_e32 v15, 0xffff0000, v225
	v_lshlrev_b32_e32 v225, 16, v225
	v_mul_f32_e32 v222, 0x3fb8aa3b, v222
	v_mul_f32_e32 v6, 0x3fb8aa3b, v6
	v_mul_f32_e32 v223, 0x3fb8aa3b, v223
	v_mul_f32_e32 v7, 0x3fb8aa3b, v7
	v_mul_f32_e32 v224, 0x3fb8aa3b, v224
	v_mul_f32_e32 v14, 0x3fb8aa3b, v14
	v_mul_f32_e32 v225, 0x3fb8aa3b, v225
	v_mul_f32_e32 v15, 0x3fb8aa3b, v15
	v_exp_f32_e32 v222, v222
	v_exp_f32_e32 v6, v6
	v_exp_f32_e32 v223, v223
	v_exp_f32_e32 v7, v7
	v_exp_f32_e32 v224, v224
	v_exp_f32_e32 v14, v14
	v_exp_f32_e32 v225, v225
	v_exp_f32_e32 v15, v15
	v_lshlrev_b32_e32 v124, 16, v226
	v_and_b32_e32 v125, 0xffff0000, v226
	v_fmac_f32_e32 v124, v122, v222
	v_fmac_f32_e32 v125, v123, v6
	v_lshlrev_b32_e32 v126, 16, v227
	v_and_b32_e32 v127, 0xffff0000, v227
	v_fmac_f32_e32 v126, v124, v223
	v_fmac_f32_e32 v127, v125, v7
	v_lshlrev_b32_e32 v128, 16, v228
	v_and_b32_e32 v129, 0xffff0000, v228
	v_fmac_f32_e32 v128, v126, v224
	v_fmac_f32_e32 v129, v127, v14
	v_lshlrev_b32_e32 v130, 16, v229
	v_and_b32_e32 v131, 0xffff0000, v229
	v_fmac_f32_e32 v130, v128, v225
	v_fmac_f32_e32 v131, v129, v15
	global_load_dwordx4 v[222:225], v3, s[70:71] nt
	global_load_dwordx4 v[226:229], v3, s[72:73] nt
	v_add_u32_e32 v3, 0x2000, v3
	s_waitcnt vmcnt(6)
; __device__ __forceinline__ float bf_lo(unsigned w) { return __uint_as_float(w << 16); }
; __device__ __forceinline__ float bf_hi(unsigned w) { return __uint_as_float(w & 0xffff0000u); }
; __device__ __forceinline__ void scan_s3(CTXA) {
;     ...
;         for (int g = 0; g < 4; ++g) { unsigned wl[16], wb[16];
; #pragma unroll
;             for (int q = 0; q < 16; ++q) { const int t = g * 16 + q; wl[q] = __builtin_nontemporal_load(la0 + (size_t)t * (D / 2)); wb[q] = __builtin_nontemporal_load(bb0 + (size_t)t * (D / 2)); }
; #pragma unroll
;             for (int q = 0; q < 16; ++q) { const int t = g * 16 + q; hf0 = __expf(bf_lo(wl[q])) * hf0 + bf_lo(wb[q]); hf1 = __expf(bf_hi(wl[q])) * hf1 + bf_hi(wb[q]); fv0[t] = hf0; fv1[t] = hf1; } }
	v_permlane16_swap_b32_e32 v198, v199
	v_permlane16_swap_b32_e32 v200, v201
	v_permlane16_swap_b32_e32 v202, v203
	v_permlane16_swap_b32_e32 v204, v205
	v_permlane32_swap_b32_e32 v198, v200
	v_permlane32_swap_b32_e32 v199, v201
	v_permlane32_swap_b32_e32 v202, v204
	v_permlane32_swap_b32_e32 v203, v205
	v_and_b32_e32 v6, 0xffff0000, v198
	v_lshlrev_b32_e32 v198, 16, v198
	v_and_b32_e32 v7, 0xffff0000, v199
	v_lshlrev_b32_e32 v199, 16, v199
	v_and_b32_e32 v14, 0xffff0000, v200
	v_lshlrev_b32_e32 v200, 16, v200
	v_and_b32_e32 v15, 0xffff0000, v201
	v_lshlrev_b32_e32 v201, 16, v201
	v_mul_f32_e32 v198, 0x3fb8aa3b, v198
	v_mul_f32_e32 v6, 0x3fb8aa3b, v6
	v_mul_f32_e32 v199, 0x3fb8aa3b, v199
	v_mul_f32_e32 v7, 0x3fb8aa3b, v7
	v_mul_f32_e32 v200, 0x3fb8aa3b, v200
	v_mul_f32_e32 v14, 0x3fb8aa3b, v14
	v_mul_f32_e32 v201, 0x3fb8aa3b, v201
	v_mul_f32_e32 v15, 0x3fb8aa3b, v15
	v_exp_f32_e32 v198, v198
	v_exp_f32_e32 v6, v6
	v_exp_f32_e32 v199, v199
	v_exp_f32_e32 v7, v7
	v_exp_f32_e32 v200, v200
	v_exp_f32_e32 v14, v14
	v_exp_f32_e32 v201, v201
	v_exp_f32_e32 v15, v15
	v_lshlrev_b32_e32 v132, 16, v202
	v_and_b32_e32 v133, 0xffff0000, v202
	v_fmac_f32_e32 v132, v130, v198
	v_fmac_f32_e32 v133, v131, v6
	v_lshlrev_b32_e32 v134, 16, v203
	v_and_b32_e32 v135, 0xffff0000, v203
	v_fmac_f32_e32 v134, v132, v199
	v_fmac_f32_e32 v135, v133, v7
	v_lshlrev_b32_e32 v136, 16, v204
	v_and_b32_e32 v137, 0xffff0000, v204
	v_fmac_f32_e32 v136, v134, v200
	v_fmac_f32_e32 v137, v135, v14
	v_lshlrev_b32_e32 v138, 16, v205
	v_and_b32_e32 v139, 0xffff0000, v205
	v_fmac_f32_e32 v138, v136, v201
	v_fmac_f32_e32 v139, v137, v15
	global_load_dwordx4 v[198:201], v3, s[70:71] nt
	global_load_dwordx4 v[202:205], v3, s[72:73] nt
	v_add_u32_e32 v3, 0x2000, v3
	s_waitcnt vmcnt(6)
	v_permlane16_swap_b32_e32 v206, v207
	v_permlane16_swap_b32_e32 v208, v209
	v_permlane16_swap_b32_e32 v210, v211
	v_permlane16_swap_b32_e32 v212, v213
	v_permlane32_swap_b32_e32 v206, v208
	v_permlane32_swap_b32_e32 v207, v209
	v_permlane32_swap_b32_e32 v210, v212
	v_permlane32_swap_b32_e32 v211, v213
	v_and_b32_e32 v6, 0xffff0000, v206
	v_lshlrev_b32_e32 v206, 16, v206
	v_and_b32_e32 v7, 0xffff0000, v207
	v_lshlrev_b32_e32 v207, 16, v207
	v_and_b32_e32 v14, 0xffff0000, v208
	v_lshlrev_b32_e32 v208, 16, v208
	v_and_b32_e32 v15, 0xffff0000, v209
	v_lshlrev_b32_e32 v209, 16, v209
	v_mul_f32_e32 v206, 0x3fb8aa3b, v206
	v_mul_f32_e32 v6, 0x3fb8aa3b, v6
	v_mul_f32_e32 v207, 0x3fb8aa3b, v207
	v_mul_f32_e32 v7, 0x3fb8aa3b, v7
	v_mul_f32_e32 v208, 0x3fb8aa3b, v208
	v_mul_f32_e32 v14, 0x3fb8aa3b, v14
	v_mul_f32_e32 v209, 0x3fb8aa3b, v209
	v_mul_f32_e32 v15, 0x3fb8aa3b, v15
	v_exp_f32_e32 v206, v206
	v_exp_f32_e32 v6, v6
	v_exp_f32_e32 v207, v207
	v_exp_f32_e32 v7, v7
	v_exp_f32_e32 v208, v208
	v_exp_f32_e32 v14, v14
	v_exp_f32_e32 v209, v209
	v_exp_f32_e32 v15, v15
	v_lshlrev_b32_e32 v140, 16, v210
	v_and_b32_e32 v141, 0xffff0000, v210
	v_fmac_f32_e32 v140, v138, v206
	v_fmac_f32_e32 v141, v139, v6
	v_lshlrev_b32_e32 v142, 16, v211
	v_and_b32_e32 v143, 0xffff0000, v211
	v_fmac_f32_e32 v142, v140, v207
	v_fmac_f32_e32 v143, v141, v7
	v_lshlrev_b32_e32 v144, 16, v212
	v_and_b32_e32 v145, 0xffff0000, v212
	v_fmac_f32_e32 v144, v142, v208
	v_fmac_f32_e32 v145, v143, v14
	v_lshlrev_b32_e32 v146, 16, v213
	v_and_b32_e32 v147, 0xffff0000, v213
	v_fmac_f32_e32 v146, v144, v209
	v_fmac_f32_e32 v147, v145, v15
	global_load_dwordx4 v[206:209], v3, s[70:71] nt
	global_load_dwordx4 v[210:213], v3, s[72:73] nt
	v_add_u32_e32 v3, 0x2000, v3
	s_waitcnt vmcnt(6)
	v_permlane16_swap_b32_e32 v214, v215
	v_permlane16_swap_b32_e32 v216, v217
	v_permlane16_swap_b32_e32 v218, v219
	v_permlane16_swap_b32_e32 v220, v221
	v_permlane32_swap_b32_e32 v214, v216
	v_permlane32_swap_b32_e32 v215, v217
	v_permlane32_swap_b32_e32 v218, v220
	v_permlane32_swap_b32_e32 v219, v221
	v_and_b32_e32 v6, 0xffff0000, v214
	v_lshlrev_b32_e32 v214, 16, v214
	v_and_b32_e32 v7, 0xffff0000, v215
	v_lshlrev_b32_e32 v215, 16, v215
	v_and_b32_e32 v14, 0xffff0000, v216
	v_lshlrev_b32_e32 v216, 16, v216
	v_and_b32_e32 v15, 0xffff0000, v217
	v_lshlrev_b32_e32 v217, 16, v217
	v_mul_f32_e32 v214, 0x3fb8aa3b, v214
	v_mul_f32_e32 v6, 0x3fb8aa3b, v6
	v_mul_f32_e32 v215, 0x3fb8aa3b, v215
	v_mul_f32_e32 v7, 0x3fb8aa3b, v7
	v_mul_f32_e32 v216, 0x3fb8aa3b, v216
	v_mul_f32_e32 v14, 0x3fb8aa3b, v14
	v_mul_f32_e32 v217, 0x3fb8aa3b, v217
	v_mul_f32_e32 v15, 0x3fb8aa3b, v15
	v_exp_f32_e32 v214, v214
	v_exp_f32_e32 v6, v6
	v_exp_f32_e32 v215, v215
	v_exp_f32_e32 v7, v7
	v_exp_f32_e32 v216, v216
	v_exp_f32_e32 v14, v14
	v_exp_f32_e32 v217, v217
	v_exp_f32_e32 v15, v15
	v_lshlrev_b32_e32 v148, 16, v218
	v_and_b32_e32 v149, 0xffff0000, v218
	v_fmac_f32_e32 v148, v146, v214
	v_fmac_f32_e32 v149, v147, v6
	v_lshlrev_b32_e32 v150, 16, v219
	v_and_b32_e32 v151, 0xffff0000, v219
	v_fmac_f32_e32 v150, v148, v215
	v_fmac_f32_e32 v151, v149, v7
	v_lshlrev_b32_e32 v152, 16, v220
	v_and_b32_e32 v153, 0xffff0000, v220
	v_fmac_f32_e32 v152, v150, v216
	v_fmac_f32_e32 v153, v151, v14
	v_lshlrev_b32_e32 v154, 16, v221
	v_and_b32_e32 v155, 0xffff0000, v221
	v_fmac_f32_e32 v154, v152, v217
	v_fmac_f32_e32 v155, v153, v15
	global_load_dwordx4 v[214:217], v3, s[70:71] nt
	global_load_dwordx4 v[218:221], v3, s[72:73] nt
	v_add_u32_e32 v3, 0x2000, v3
	s_waitcnt vmcnt(6)
; __device__ __forceinline__ float bf_lo(unsigned w) { return __uint_as_float(w << 16); }
; __device__ __forceinline__ float bf_hi(unsigned w) { return __uint_as_float(w & 0xffff0000u); }
; __device__ __forceinline__ void scan_s3(CTXA) {
;     ...
;         for (int g = 0; g < 4; ++g) { unsigned wl[16], wb[16];
; #pragma unroll
;             for (int q = 0; q < 16; ++q) { const int t = g * 16 + q; wl[q] = __builtin_nontemporal_load(la0 + (size_t)t * (D / 2)); wb[q] = __builtin_nontemporal_load(bb0 + (size_t)t * (D / 2)); }
; #pragma unroll
;             for (int q = 0; q < 16; ++q) { const int t = g * 16 + q; hf0 = __expf(bf_lo(wl[q])) * hf0 + bf_lo(wb[q]); hf1 = __expf(bf_hi(wl[q])) * hf1 + bf_hi(wb[q]); fv0[t] = hf0; fv1[t] = hf1; } }
	v_permlane16_swap_b32_e32 v222, v223
	v_permlane16_swap_b32_e32 v224, v225
	v_permlane16_swap_b32_e32 v226, v227
	v_permlane16_swap_b32_e32 v228, v229
	v_permlane32_swap_b32_e32 v222, v224
	v_permlane32_swap_b32_e32 v223, v225
	v_permlane32_swap_b32_e32 v226, v228
	v_permlane32_swap_b32_e32 v227, v229
	v_and_b32_e32 v6, 0xffff0000, v222
	v_lshlrev_b32_e32 v222, 16, v222
	v_and_b32_e32 v7, 0xffff0000, v223
	v_lshlrev_b32_e32 v223, 16, v223
	v_and_b32_e32 v14, 0xffff0000, v224
	v_lshlrev_b32_e32 v224, 16, v224
	v_and_b32_e32 v15, 0xffff0000, v225
	v_lshlrev_b32_e32 v225, 16, v225
	v_mul_f32_e32 v222, 0x3fb8aa3b, v222
	v_mul_f32_e32 v6, 0x3fb8aa3b, v6
	v_mul_f32_e32 v223, 0x3fb8aa3b, v223
	v_mul_f32_e32 v7, 0x3fb8aa3b, v7
	v_mul_f32_e32 v224, 0x3fb8aa3b, v224
	v_mul_f32_e32 v14, 0x3fb8aa3b, v14
	v_mul_f32_e32 v225, 0x3fb8aa3b, v225
	v_mul_f32_e32 v15, 0x3fb8aa3b, v15
	v_exp_f32_e32 v222, v222
	v_exp_f32_e32 v6, v6
	v_exp_f32_e32 v223, v223
	v_exp_f32_e32 v7, v7
	v_exp_f32_e32 v224, v224
	v_exp_f32_e32 v14, v14
	v_exp_f32_e32 v225, v225
	v_exp_f32_e32 v15, v15
	v_lshlrev_b32_e32 v156, 16, v226
	v_and_b32_e32 v157, 0xffff0000, v226
	v_fmac_f32_e32 v156, v154, v222
	v_fmac_f32_e32 v157, v155, v6
	v_lshlrev_b32_e32 v158, 16, v227
	v_and_b32_e32 v159, 0xffff0000, v227
	v_fmac_f32_e32 v158, v156, v223
	v_fmac_f32_e32 v159, v157, v7
	v_lshlrev_b32_e32 v160, 16, v228
	v_and_b32_e32 v161, 0xffff0000, v228
	v_fmac_f32_e32 v160, v158, v224
	v_fmac_f32_e32 v161, v159, v14
	v_lshlrev_b32_e32 v162, 16, v229
	v_and_b32_e32 v163, 0xffff0000, v229
	v_fmac_f32_e32 v162, v160, v225
	v_fmac_f32_e32 v163, v161, v15
	global_load_dwordx4 v[222:225], v3, s[70:71] nt
	global_load_dwordx4 v[226:229], v3, s[72:73] nt
	s_waitcnt vmcnt(6)
	v_permlane16_swap_b32_e32 v198, v199
	v_permlane16_swap_b32_e32 v200, v201
	v_permlane16_swap_b32_e32 v202, v203
	v_permlane16_swap_b32_e32 v204, v205
	v_permlane32_swap_b32_e32 v198, v200
	v_permlane32_swap_b32_e32 v199, v201
	v_permlane32_swap_b32_e32 v202, v204
	v_permlane32_swap_b32_e32 v203, v205
	v_and_b32_e32 v6, 0xffff0000, v198
	v_lshlrev_b32_e32 v198, 16, v198
	v_and_b32_e32 v7, 0xffff0000, v199
	v_lshlrev_b32_e32 v199, 16, v199
	v_and_b32_e32 v14, 0xffff0000, v200
	v_lshlrev_b32_e32 v200, 16, v200
	v_and_b32_e32 v15, 0xffff0000, v201
	v_lshlrev_b32_e32 v201, 16, v201
	v_mul_f32_e32 v198, 0x3fb8aa3b, v198
	v_mul_f32_e32 v6, 0x3fb8aa3b, v6
	v_mul_f32_e32 v199, 0x3fb8aa3b, v199
	v_mul_f32_e32 v7, 0x3fb8aa3b, v7
	v_mul_f32_e32 v200, 0x3fb8aa3b, v200
	v_mul_f32_e32 v14, 0x3fb8aa3b, v14
	v_mul_f32_e32 v201, 0x3fb8aa3b, v201
	v_mul_f32_e32 v15, 0x3fb8aa3b, v15
	v_exp_f32_e32 v198, v198
	v_exp_f32_e32 v6, v6
	v_exp_f32_e32 v199, v199
	v_exp_f32_e32 v7, v7
	v_exp_f32_e32 v200, v200
	v_exp_f32_e32 v14, v14
	v_exp_f32_e32 v201, v201
	v_exp_f32_e32 v15, v15
	v_lshlrev_b32_e32 v164, 16, v202
	v_and_b32_e32 v165, 0xffff0000, v202
	v_fmac_f32_e32 v164, v162, v198
	v_fmac_f32_e32 v165, v163, v6
	v_lshlrev_b32_e32 v166, 16, v203
	v_and_b32_e32 v167, 0xffff0000, v203
	v_fmac_f32_e32 v166, v164, v199
	v_fmac_f32_e32 v167, v165, v7
	v_lshlrev_b32_e32 v168, 16, v204
	v_and_b32_e32 v169, 0xffff0000, v204
	v_fmac_f32_e32 v168, v166, v200
	v_fmac_f32_e32 v169, v167, v14
	v_lshlrev_b32_e32 v170, 16, v205
	v_and_b32_e32 v171, 0xffff0000, v205
	v_fmac_f32_e32 v170, v168, v201
	v_fmac_f32_e32 v171, v169, v15
	s_waitcnt vmcnt(4)
	v_permlane16_swap_b32_e32 v206, v207
	v_permlane16_swap_b32_e32 v208, v209
	v_permlane16_swap_b32_e32 v210, v211
	v_permlane16_swap_b32_e32 v212, v213
	v_permlane32_swap_b32_e32 v206, v208
	v_permlane32_swap_b32_e32 v207, v209
	v_permlane32_swap_b32_e32 v210, v212
	v_permlane32_swap_b32_e32 v211, v213
	v_and_b32_e32 v6, 0xffff0000, v206
	v_lshlrev_b32_e32 v206, 16, v206
	v_and_b32_e32 v7, 0xffff0000, v207
	v_lshlrev_b32_e32 v207, 16, v207
	v_and_b32_e32 v14, 0xffff0000, v208
	v_lshlrev_b32_e32 v208, 16, v208
	v_and_b32_e32 v15, 0xffff0000, v209
	v_lshlrev_b32_e32 v209, 16, v209
	v_mul_f32_e32 v206, 0x3fb8aa3b, v206
	v_mul_f32_e32 v6, 0x3fb8aa3b, v6
	v_mul_f32_e32 v207, 0x3fb8aa3b, v207
	v_mul_f32_e32 v7, 0x3fb8aa3b, v7
	v_mul_f32_e32 v208, 0x3fb8aa3b, v208
	v_mul_f32_e32 v14, 0x3fb8aa3b, v14
	v_mul_f32_e32 v209, 0x3fb8aa3b, v209
	v_mul_f32_e32 v15, 0x3fb8aa3b, v15
	v_exp_f32_e32 v206, v206
	v_exp_f32_e32 v6, v6
	v_exp_f32_e32 v207, v207
	v_exp_f32_e32 v7, v7
	v_exp_f32_e32 v208, v208
	v_exp_f32_e32 v14, v14
	v_exp_f32_e32 v209, v209
	v_exp_f32_e32 v15, v15
	v_lshlrev_b32_e32 v172, 16, v210
	v_and_b32_e32 v173, 0xffff0000, v210
	v_fmac_f32_e32 v172, v170, v206
	v_fmac_f32_e32 v173, v171, v6
	v_lshlrev_b32_e32 v174, 16, v211
	v_and_b32_e32 v175, 0xffff0000, v211
	v_fmac_f32_e32 v174, v172, v207
	v_fmac_f32_e32 v175, v173, v7
	v_lshlrev_b32_e32 v176, 16, v212
	v_and_b32_e32 v177, 0xffff0000, v212
	v_fmac_f32_e32 v176, v174, v208
	v_fmac_f32_e32 v177, v175, v14
	v_lshlrev_b32_e32 v178, 16, v213
	v_and_b32_e32 v179, 0xffff0000, v213
	v_fmac_f32_e32 v178, v176, v209
	v_fmac_f32_e32 v179, v177, v15
	s_waitcnt vmcnt(2)
; __device__ __forceinline__ unsigned cvt_pk_bf16(float lo, float hi) { unsigned r; asm("v_cvt_pk_bf16_f32 %0, %1, %2" : "=v"(r) : "v"(lo), "v"(hi)); return r; }
; __device__ __forceinline__ float bf_lo(unsigned w) { return __uint_as_float(w << 16); }
; __device__ __forceinline__ float bf_hi(unsigned w) { return __uint_as_float(w & 0xffff0000u); }
; __device__ __forceinline__ void scan_s3(CTXA) {
;     ...
;         for (int g = 0; g < 4; ++g) { unsigned wl[16], wb[16];
; #pragma unroll
;             for (int q = 0; q < 16; ++q) { const int t = g * 16 + q; wl[q] = __builtin_nontemporal_load(la0 + (size_t)t * (D / 2)); wb[q] = __builtin_nontemporal_load(bb0 + (size_t)t * (D / 2)); }
; #pragma unroll
;             for (int q = 0; q < 16; ++q) { const int t = g * 16 + q; hf0 = __expf(bf_lo(wl[q])) * hf0 + bf_lo(wb[q]); hf1 = __expf(bf_hi(wl[q])) * hf1 + bf_hi(wb[q]); fv0[t] = hf0; fv1[t] = hf1; } }
; #pragma unroll
;         for (int g = 0; g < 4; ++g) { unsigned wl[16], wb[16], wg[16];
; #pragma unroll
;             for (int q = 0; q < 16; ++q) { const int t = 63 - (g * 16 + q); wl[q] = __builtin_nontemporal_load(la1 + (size_t)t * (D / 2)); wb[q] = __builtin_nontemporal_load(bb1 + (size_t)t * (D / 2)); wg[q] = __builtin_nontemporal_load(gg + (size_t)t * (D / 2)); }
; #pragma unroll
;             for (int q = 0; q < 16; ++q) { const int t = 63 - (g * 16 + q); hb0 = __expf(bf_lo(wl[q])) * hb0 + bf_lo(wb[q]); hb1 = __expf(bf_hi(wl[q])) * hb1 + bf_hi(wb[q]);
;                 yy[(size_t)t * (D / 2)] = cvt_pk_bf16((fv0[t] + hb0) * bf_lo(wg[q]), (fv1[t] + hb1) * bf_hi(wg[q])); } }
	v_permlane16_swap_b32_e32 v214, v215
	v_permlane16_swap_b32_e32 v216, v217
	v_permlane16_swap_b32_e32 v218, v219
	v_permlane16_swap_b32_e32 v220, v221
	v_permlane32_swap_b32_e32 v214, v216
	v_permlane32_swap_b32_e32 v215, v217
	v_permlane32_swap_b32_e32 v218, v220
	v_permlane32_swap_b32_e32 v219, v221
	v_and_b32_e32 v6, 0xffff0000, v214
	v_lshlrev_b32_e32 v214, 16, v214
	v_and_b32_e32 v7, 0xffff0000, v215
	v_lshlrev_b32_e32 v215, 16, v215
	v_and_b32_e32 v14, 0xffff0000, v216
	v_lshlrev_b32_e32 v216, 16, v216
	v_and_b32_e32 v15, 0xffff0000, v217
	v_lshlrev_b32_e32 v217, 16, v217
	v_mul_f32_e32 v214, 0x3fb8aa3b, v214
	v_mul_f32_e32 v6, 0x3fb8aa3b, v6
	v_mul_f32_e32 v215, 0x3fb8aa3b, v215
	v_mul_f32_e32 v7, 0x3fb8aa3b, v7
	v_mul_f32_e32 v216, 0x3fb8aa3b, v216
	v_mul_f32_e32 v14, 0x3fb8aa3b, v14
	v_mul_f32_e32 v217, 0x3fb8aa3b, v217
	v_mul_f32_e32 v15, 0x3fb8aa3b, v15
	v_exp_f32_e32 v214, v214
	v_exp_f32_e32 v6, v6
	v_exp_f32_e32 v215, v215
	v_exp_f32_e32 v7, v7
	v_exp_f32_e32 v216, v216
	v_exp_f32_e32 v14, v14
	v_exp_f32_e32 v217, v217
	v_exp_f32_e32 v15, v15
	v_lshlrev_b32_e32 v180, 16, v218
	v_and_b32_e32 v181, 0xffff0000, v218
	v_fmac_f32_e32 v180, v178, v214
	v_fmac_f32_e32 v181, v179, v6
	v_lshlrev_b32_e32 v182, 16, v219
	v_and_b32_e32 v183, 0xffff0000, v219
	v_fmac_f32_e32 v182, v180, v215
	v_fmac_f32_e32 v183, v181, v7
	v_lshlrev_b32_e32 v184, 16, v220
	v_and_b32_e32 v185, 0xffff0000, v220
	v_fmac_f32_e32 v184, v182, v216
	v_fmac_f32_e32 v185, v183, v14
	v_lshlrev_b32_e32 v186, 16, v221
	v_and_b32_e32 v187, 0xffff0000, v221
	v_fmac_f32_e32 v186, v184, v217
	v_fmac_f32_e32 v187, v185, v15
	s_waitcnt vmcnt(0)
	v_permlane16_swap_b32_e32 v222, v223
	v_permlane16_swap_b32_e32 v224, v225
	v_permlane16_swap_b32_e32 v226, v227
	v_permlane16_swap_b32_e32 v228, v229
	v_permlane32_swap_b32_e32 v222, v224
	v_permlane32_swap_b32_e32 v223, v225
	v_permlane32_swap_b32_e32 v226, v228
	v_permlane32_swap_b32_e32 v227, v229
	v_and_b32_e32 v6, 0xffff0000, v222
	v_lshlrev_b32_e32 v222, 16, v222
	v_and_b32_e32 v7, 0xffff0000, v223
	v_lshlrev_b32_e32 v223, 16, v223
	v_and_b32_e32 v14, 0xffff0000, v224
	v_lshlrev_b32_e32 v224, 16, v224
	v_and_b32_e32 v15, 0xffff0000, v225
	v_lshlrev_b32_e32 v225, 16, v225
	v_mul_f32_e32 v222, 0x3fb8aa3b, v222
	v_mul_f32_e32 v6, 0x3fb8aa3b, v6
	v_mul_f32_e32 v223, 0x3fb8aa3b, v223
	v_mul_f32_e32 v7, 0x3fb8aa3b, v7
	v_mul_f32_e32 v224, 0x3fb8aa3b, v224
	v_mul_f32_e32 v14, 0x3fb8aa3b, v14
	v_mul_f32_e32 v225, 0x3fb8aa3b, v225
	v_mul_f32_e32 v15, 0x3fb8aa3b, v15
	v_exp_f32_e32 v222, v222
	v_exp_f32_e32 v6, v6
	v_exp_f32_e32 v223, v223
	v_exp_f32_e32 v7, v7
	v_exp_f32_e32 v224, v224
	v_exp_f32_e32 v14, v14
	v_exp_f32_e32 v225, v225
	v_exp_f32_e32 v15, v15
	v_lshlrev_b32_e32 v188, 16, v226
	v_and_b32_e32 v189, 0xffff0000, v226
	v_fmac_f32_e32 v188, v186, v222
	v_fmac_f32_e32 v189, v187, v6
	v_lshlrev_b32_e32 v190, 16, v227
	v_and_b32_e32 v191, 0xffff0000, v227
	v_fmac_f32_e32 v190, v188, v223
	v_fmac_f32_e32 v191, v189, v7
	v_lshlrev_b32_e32 v192, 16, v228
	v_and_b32_e32 v193, 0xffff0000, v228
	v_fmac_f32_e32 v192, v190, v224
	v_fmac_f32_e32 v193, v191, v14
	v_lshlrev_b32_e32 v194, 16, v229
	v_and_b32_e32 v195, 0xffff0000, v229
	v_fmac_f32_e32 v194, v192, v225
	v_fmac_f32_e32 v195, v193, v15
	s_waitcnt vmcnt(33)
	v_permlane16_swap_b32_e32 v18, v19
	v_permlane16_swap_b32_e32 v20, v21
	v_permlane16_swap_b32_e32 v22, v23
	v_permlane16_swap_b32_e32 v24, v25
	v_permlane16_swap_b32_e32 v26, v27
	v_permlane16_swap_b32_e32 v28, v29
	v_permlane32_swap_b32_e32 v18, v20
	v_permlane32_swap_b32_e32 v19, v21
	v_permlane32_swap_b32_e32 v22, v24
	v_permlane32_swap_b32_e32 v23, v25
	v_permlane32_swap_b32_e32 v26, v28
	v_permlane32_swap_b32_e32 v27, v29
	v_and_b32_e32 v6, 0xffff0000, v18
	v_lshlrev_b32_e32 v18, 16, v18
	v_and_b32_e32 v7, 0xffff0000, v19
	v_lshlrev_b32_e32 v19, 16, v19
	v_and_b32_e32 v14, 0xffff0000, v20
	v_lshlrev_b32_e32 v20, 16, v20
	v_and_b32_e32 v15, 0xffff0000, v21
	v_lshlrev_b32_e32 v21, 16, v21
	v_mul_f32_e32 v18, 0x3fb8aa3b, v18
	v_mul_f32_e32 v6, 0x3fb8aa3b, v6
	v_mul_f32_e32 v19, 0x3fb8aa3b, v19
	v_mul_f32_e32 v7, 0x3fb8aa3b, v7
	v_mul_f32_e32 v20, 0x3fb8aa3b, v20
	v_mul_f32_e32 v14, 0x3fb8aa3b, v14
	v_mul_f32_e32 v21, 0x3fb8aa3b, v21
	v_mul_f32_e32 v15, 0x3fb8aa3b, v15
	v_exp_f32_e32 v18, v18
	v_exp_f32_e32 v6, v6
	v_exp_f32_e32 v19, v19
	v_exp_f32_e32 v7, v7
	v_exp_f32_e32 v20, v20
	v_exp_f32_e32 v14, v14
	v_exp_f32_e32 v21, v21
	v_exp_f32_e32 v15, v15
	v_lshlrev_b32_e32 v12, 16, v25
	v_and_b32_e32 v13, 0xffff0000, v25
	v_fmac_f32_e32 v12, v10, v21
	v_fmac_f32_e32 v13, v11, v15
	v_lshlrev_b32_e32 v17, 16, v29
	v_and_b32_e32 v29, 0xffff0000, v29
	v_add_f32_e32 v194, v194, v12
	v_add_f32_e32 v195, v195, v13
	v_mul_f32_e32 v194, v194, v17
	v_mul_f32_e32 v195, v195, v29
	v_cvt_pk_bf16_f32 v29, v194, v195
	v_lshlrev_b32_e32 v10, 16, v24
	v_and_b32_e32 v11, 0xffff0000, v24
	v_fmac_f32_e32 v10, v12, v20
	v_fmac_f32_e32 v11, v13, v14
	v_lshlrev_b32_e32 v17, 16, v28
	v_and_b32_e32 v28, 0xffff0000, v28
	v_add_f32_e32 v192, v192, v10
	v_add_f32_e32 v193, v193, v11
	v_mul_f32_e32 v192, v192, v17
	v_mul_f32_e32 v193, v193, v28
	v_cvt_pk_bf16_f32 v28, v192, v193
	v_lshlrev_b32_e32 v12, 16, v23
	v_and_b32_e32 v13, 0xffff0000, v23
	v_fmac_f32_e32 v12, v10, v19
	v_fmac_f32_e32 v13, v11, v7
	v_lshlrev_b32_e32 v17, 16, v27
	v_and_b32_e32 v27, 0xffff0000, v27
	v_add_f32_e32 v190, v190, v12
	v_add_f32_e32 v191, v191, v13
	v_mul_f32_e32 v190, v190, v17
	v_mul_f32_e32 v191, v191, v27
	v_cvt_pk_bf16_f32 v27, v190, v191
	v_lshlrev_b32_e32 v10, 16, v22
	v_and_b32_e32 v11, 0xffff0000, v22
	v_fmac_f32_e32 v10, v12, v18
	v_fmac_f32_e32 v11, v13, v6
	v_lshlrev_b32_e32 v17, 16, v26
	v_and_b32_e32 v26, 0xffff0000, v26
	v_add_f32_e32 v188, v188, v10
	v_add_f32_e32 v189, v189, v11
	v_mul_f32_e32 v188, v188, v17
	v_mul_f32_e32 v189, v189, v26
	v_cvt_pk_bf16_f32 v26, v188, v189
	s_nop 1
	v_permlane16_swap_b32_e32 v26, v27
	v_permlane16_swap_b32_e32 v28, v29
	s_nop 1
	v_permlane32_swap_b32_e32 v26, v28
	v_permlane32_swap_b32_e32 v27, v29
	global_store_dwordx4 v5, v[26:29], s[80:81]
	v_add_u32_e32 v5, 0xffffe000, v5
	global_load_dwordx4 v[18:21], v4, s[82:83] nt
	global_load_dwordx4 v[22:25], v4, s[84:85] nt
	global_load_dwordx4 v[26:29], v4, s[78:79] nt
	v_add_u32_e32 v4, 0xffffe000, v4
	s_waitcnt vmcnt(34)
; __device__ __forceinline__ unsigned cvt_pk_bf16(float lo, float hi) { unsigned r; asm("v_cvt_pk_bf16_f32 %0, %1, %2" : "=v"(r) : "v"(lo), "v"(hi)); return r; }
; __device__ __forceinline__ float bf_lo(unsigned w) { return __uint_as_float(w << 16); }
; __device__ __forceinline__ float bf_hi(unsigned w) { return __uint_as_float(w & 0xffff0000u); }
; __device__ __forceinline__ void scan_s3(CTXA) {
;     ...
;         for (int g = 0; g < 4; ++g) { unsigned wl[16], wb[16], wg[16];
; #pragma unroll
;             for (int q = 0; q < 16; ++q) { const int t = 63 - (g * 16 + q); wl[q] = __builtin_nontemporal_load(la1 + (size_t)t * (D / 2)); wb[q] = __builtin_nontemporal_load(bb1 + (size_t)t * (D / 2)); wg[q] = __builtin_nontemporal_load(gg + (size_t)t * (D / 2)); }
; #pragma unroll
;             for (int q = 0; q < 16; ++q) { const int t = 63 - (g * 16 + q); hb0 = __expf(bf_lo(wl[q])) * hb0 + bf_lo(wb[q]); hb1 = __expf(bf_hi(wl[q])) * hb1 + bf_hi(wb[q]);
;                 yy[(size_t)t * (D / 2)] = cvt_pk_bf16((fv0[t] + hb0) * bf_lo(wg[q]), (fv1[t] + hb1) * bf_hi(wg[q])); } }
	v_permlane16_swap_b32_e32 v30, v31
	v_permlane16_swap_b32_e32 v32, v33
	v_permlane16_swap_b32_e32 v34, v35
	v_permlane16_swap_b32_e32 v36, v37
	v_permlane16_swap_b32_e32 v38, v39
	v_permlane16_swap_b32_e32 v40, v41
	v_permlane32_swap_b32_e32 v30, v32
	v_permlane32_swap_b32_e32 v31, v33
	v_permlane32_swap_b32_e32 v34, v36
	v_permlane32_swap_b32_e32 v35, v37
	v_permlane32_swap_b32_e32 v38, v40
	v_permlane32_swap_b32_e32 v39, v41
	v_and_b32_e32 v6, 0xffff0000, v30
	v_lshlrev_b32_e32 v30, 16, v30
	v_and_b32_e32 v7, 0xffff0000, v31
	v_lshlrev_b32_e32 v31, 16, v31
	v_and_b32_e32 v14, 0xffff0000, v32
	v_lshlrev_b32_e32 v32, 16, v32
	v_and_b32_e32 v15, 0xffff0000, v33
	v_lshlrev_b32_e32 v33, 16, v33
	v_mul_f32_e32 v30, 0x3fb8aa3b, v30
	v_mul_f32_e32 v6, 0x3fb8aa3b, v6
	v_mul_f32_e32 v31, 0x3fb8aa3b, v31
	v_mul_f32_e32 v7, 0x3fb8aa3b, v7
	v_mul_f32_e32 v32, 0x3fb8aa3b, v32
	v_mul_f32_e32 v14, 0x3fb8aa3b, v14
	v_mul_f32_e32 v33, 0x3fb8aa3b, v33
	v_mul_f32_e32 v15, 0x3fb8aa3b, v15
	v_exp_f32_e32 v30, v30
	v_exp_f32_e32 v6, v6
	v_exp_f32_e32 v31, v31
	v_exp_f32_e32 v7, v7
	v_exp_f32_e32 v32, v32
	v_exp_f32_e32 v14, v14
	v_exp_f32_e32 v33, v33
	v_exp_f32_e32 v15, v15
	v_lshlrev_b32_e32 v12, 16, v37
	v_and_b32_e32 v13, 0xffff0000, v37
	v_fmac_f32_e32 v12, v10, v33
	v_fmac_f32_e32 v13, v11, v15
	v_lshlrev_b32_e32 v17, 16, v41
	v_and_b32_e32 v41, 0xffff0000, v41
	v_add_f32_e32 v186, v186, v12
	v_add_f32_e32 v187, v187, v13
	v_mul_f32_e32 v186, v186, v17
	v_mul_f32_e32 v187, v187, v41
	v_cvt_pk_bf16_f32 v41, v186, v187
	v_lshlrev_b32_e32 v10, 16, v36
	v_and_b32_e32 v11, 0xffff0000, v36
	v_fmac_f32_e32 v10, v12, v32
	v_fmac_f32_e32 v11, v13, v14
	v_lshlrev_b32_e32 v17, 16, v40
	v_and_b32_e32 v40, 0xffff0000, v40
	v_add_f32_e32 v184, v184, v10
	v_add_f32_e32 v185, v185, v11
	v_mul_f32_e32 v184, v184, v17
	v_mul_f32_e32 v185, v185, v40
	v_cvt_pk_bf16_f32 v40, v184, v185
	v_lshlrev_b32_e32 v12, 16, v35
	v_and_b32_e32 v13, 0xffff0000, v35
	v_fmac_f32_e32 v12, v10, v31
	v_fmac_f32_e32 v13, v11, v7
	v_lshlrev_b32_e32 v17, 16, v39
	v_and_b32_e32 v39, 0xffff0000, v39
	v_add_f32_e32 v182, v182, v12
	v_add_f32_e32 v183, v183, v13
	v_mul_f32_e32 v182, v182, v17
	v_mul_f32_e32 v183, v183, v39
	v_cvt_pk_bf16_f32 v39, v182, v183
	v_lshlrev_b32_e32 v10, 16, v34
	v_and_b32_e32 v11, 0xffff0000, v34
	v_fmac_f32_e32 v10, v12, v30
	v_fmac_f32_e32 v11, v13, v6
	v_lshlrev_b32_e32 v17, 16, v38
	v_and_b32_e32 v38, 0xffff0000, v38
	v_add_f32_e32 v180, v180, v10
	v_add_f32_e32 v181, v181, v11
	v_mul_f32_e32 v180, v180, v17
	v_mul_f32_e32 v181, v181, v38
	v_cvt_pk_bf16_f32 v38, v180, v181
	s_nop 1
	v_permlane16_swap_b32_e32 v38, v39
	v_permlane16_swap_b32_e32 v40, v41
	s_nop 1
	v_permlane32_swap_b32_e32 v38, v40
	v_permlane32_swap_b32_e32 v39, v41
	global_store_dwordx4 v5, v[38:41], s[80:81]
	v_add_u32_e32 v5, 0xffffe000, v5
	global_load_dwordx4 v[30:33], v4, s[82:83] nt
	global_load_dwordx4 v[34:37], v4, s[84:85] nt
	global_load_dwordx4 v[38:41], v4, s[78:79] nt
	v_add_u32_e32 v4, 0xffffe000, v4
	s_waitcnt vmcnt(35)
	v_permlane16_swap_b32_e32 v42, v43
	v_permlane16_swap_b32_e32 v44, v45
	v_permlane16_swap_b32_e32 v46, v47
	v_permlane16_swap_b32_e32 v48, v49
	v_permlane16_swap_b32_e32 v50, v51
	v_permlane16_swap_b32_e32 v52, v53
	v_permlane32_swap_b32_e32 v42, v44
	v_permlane32_swap_b32_e32 v43, v45
	v_permlane32_swap_b32_e32 v46, v48
	v_permlane32_swap_b32_e32 v47, v49
	v_permlane32_swap_b32_e32 v50, v52
	v_permlane32_swap_b32_e32 v51, v53
	v_and_b32_e32 v6, 0xffff0000, v42
	v_lshlrev_b32_e32 v42, 16, v42
	v_and_b32_e32 v7, 0xffff0000, v43
	v_lshlrev_b32_e32 v43, 16, v43
	v_and_b32_e32 v14, 0xffff0000, v44
	v_lshlrev_b32_e32 v44, 16, v44
	v_and_b32_e32 v15, 0xffff0000, v45
	v_lshlrev_b32_e32 v45, 16, v45
	v_mul_f32_e32 v42, 0x3fb8aa3b, v42
	v_mul_f32_e32 v6, 0x3fb8aa3b, v6
	v_mul_f32_e32 v43, 0x3fb8aa3b, v43
	v_mul_f32_e32 v7, 0x3fb8aa3b, v7
	v_mul_f32_e32 v44, 0x3fb8aa3b, v44
	v_mul_f32_e32 v14, 0x3fb8aa3b, v14
	v_mul_f32_e32 v45, 0x3fb8aa3b, v45
	v_mul_f32_e32 v15, 0x3fb8aa3b, v15
	v_exp_f32_e32 v42, v42
	v_exp_f32_e32 v6, v6
	v_exp_f32_e32 v43, v43
	v_exp_f32_e32 v7, v7
	v_exp_f32_e32 v44, v44
	v_exp_f32_e32 v14, v14
	v_exp_f32_e32 v45, v45
	v_exp_f32_e32 v15, v15
	v_lshlrev_b32_e32 v12, 16, v49
	v_and_b32_e32 v13, 0xffff0000, v49
	v_fmac_f32_e32 v12, v10, v45
	v_fmac_f32_e32 v13, v11, v15
	v_lshlrev_b32_e32 v17, 16, v53
	v_and_b32_e32 v53, 0xffff0000, v53
	v_add_f32_e32 v178, v178, v12
	v_add_f32_e32 v179, v179, v13
	v_mul_f32_e32 v178, v178, v17
	v_mul_f32_e32 v179, v179, v53
	v_cvt_pk_bf16_f32 v53, v178, v179
	v_lshlrev_b32_e32 v10, 16, v48
	v_and_b32_e32 v11, 0xffff0000, v48
	v_fmac_f32_e32 v10, v12, v44
	v_fmac_f32_e32 v11, v13, v14
	v_lshlrev_b32_e32 v17, 16, v52
	v_and_b32_e32 v52, 0xffff0000, v52
	v_add_f32_e32 v176, v176, v10
	v_add_f32_e32 v177, v177, v11
	v_mul_f32_e32 v176, v176, v17
	v_mul_f32_e32 v177, v177, v52
	v_cvt_pk_bf16_f32 v52, v176, v177
	v_lshlrev_b32_e32 v12, 16, v47
	v_and_b32_e32 v13, 0xffff0000, v47
	v_fmac_f32_e32 v12, v10, v43
	v_fmac_f32_e32 v13, v11, v7
	v_lshlrev_b32_e32 v17, 16, v51
	v_and_b32_e32 v51, 0xffff0000, v51
	v_add_f32_e32 v174, v174, v12
	v_add_f32_e32 v175, v175, v13
	v_mul_f32_e32 v174, v174, v17
	v_mul_f32_e32 v175, v175, v51
	v_cvt_pk_bf16_f32 v51, v174, v175
	v_lshlrev_b32_e32 v10, 16, v46
	v_and_b32_e32 v11, 0xffff0000, v46
	v_fmac_f32_e32 v10, v12, v42
	v_fmac_f32_e32 v11, v13, v6
	v_lshlrev_b32_e32 v17, 16, v50
	v_and_b32_e32 v50, 0xffff0000, v50
	v_add_f32_e32 v172, v172, v10
	v_add_f32_e32 v173, v173, v11
	v_mul_f32_e32 v172, v172, v17
	v_mul_f32_e32 v173, v173, v50
	v_cvt_pk_bf16_f32 v50, v172, v173
	s_nop 1
	v_permlane16_swap_b32_e32 v50, v51
	v_permlane16_swap_b32_e32 v52, v53
	s_nop 1
	v_permlane32_swap_b32_e32 v50, v52
	v_permlane32_swap_b32_e32 v51, v53
	global_store_dwordx4 v5, v[50:53], s[80:81]
	v_add_u32_e32 v5, 0xffffe000, v5
	global_load_dwordx4 v[42:45], v4, s[82:83] nt
	global_load_dwordx4 v[46:49], v4, s[84:85] nt
	global_load_dwordx4 v[50:53], v4, s[78:79] nt
	v_add_u32_e32 v4, 0xffffe000, v4
	s_waitcnt vmcnt(36)
; __device__ __forceinline__ unsigned cvt_pk_bf16(float lo, float hi) { unsigned r; asm("v_cvt_pk_bf16_f32 %0, %1, %2" : "=v"(r) : "v"(lo), "v"(hi)); return r; }
; __device__ __forceinline__ float bf_lo(unsigned w) { return __uint_as_float(w << 16); }
; __device__ __forceinline__ float bf_hi(unsigned w) { return __uint_as_float(w & 0xffff0000u); }
; __device__ __forceinline__ void scan_s3(CTXA) {
;     ...
;         for (int g = 0; g < 4; ++g) { unsigned wl[16], wb[16], wg[16];
; #pragma unroll
;             for (int q = 0; q < 16; ++q) { const int t = 63 - (g * 16 + q); wl[q] = __builtin_nontemporal_load(la1 + (size_t)t * (D / 2)); wb[q] = __builtin_nontemporal_load(bb1 + (size_t)t * (D / 2)); wg[q] = __builtin_nontemporal_load(gg + (size_t)t * (D / 2)); }
; #pragma unroll
;             for (int q = 0; q < 16; ++q) { const int t = 63 - (g * 16 + q); hb0 = __expf(bf_lo(wl[q])) * hb0 + bf_lo(wb[q]); hb1 = __expf(bf_hi(wl[q])) * hb1 + bf_hi(wb[q]);
;                 yy[(size_t)t * (D / 2)] = cvt_pk_bf16((fv0[t] + hb0) * bf_lo(wg[q]), (fv1[t] + hb1) * bf_hi(wg[q])); } }
	v_permlane16_swap_b32_e32 v54, v55
	v_permlane16_swap_b32_e32 v56, v57
	v_permlane16_swap_b32_e32 v58, v59
	v_permlane16_swap_b32_e32 v60, v61
	v_permlane16_swap_b32_e32 v62, v63
	v_permlane16_swap_b32_e32 v64, v65
	v_permlane32_swap_b32_e32 v54, v56
	v_permlane32_swap_b32_e32 v55, v57
	v_permlane32_swap_b32_e32 v58, v60
	v_permlane32_swap_b32_e32 v59, v61
	v_permlane32_swap_b32_e32 v62, v64
	v_permlane32_swap_b32_e32 v63, v65
	v_and_b32_e32 v6, 0xffff0000, v54
	v_lshlrev_b32_e32 v54, 16, v54
	v_and_b32_e32 v7, 0xffff0000, v55
	v_lshlrev_b32_e32 v55, 16, v55
	v_and_b32_e32 v14, 0xffff0000, v56
	v_lshlrev_b32_e32 v56, 16, v56
	v_and_b32_e32 v15, 0xffff0000, v57
	v_lshlrev_b32_e32 v57, 16, v57
	v_mul_f32_e32 v54, 0x3fb8aa3b, v54
	v_mul_f32_e32 v6, 0x3fb8aa3b, v6
	v_mul_f32_e32 v55, 0x3fb8aa3b, v55
	v_mul_f32_e32 v7, 0x3fb8aa3b, v7
	v_mul_f32_e32 v56, 0x3fb8aa3b, v56
	v_mul_f32_e32 v14, 0x3fb8aa3b, v14
	v_mul_f32_e32 v57, 0x3fb8aa3b, v57
	v_mul_f32_e32 v15, 0x3fb8aa3b, v15
	v_exp_f32_e32 v54, v54
	v_exp_f32_e32 v6, v6
	v_exp_f32_e32 v55, v55
	v_exp_f32_e32 v7, v7
	v_exp_f32_e32 v56, v56
	v_exp_f32_e32 v14, v14
	v_exp_f32_e32 v57, v57
	v_exp_f32_e32 v15, v15
	v_lshlrev_b32_e32 v12, 16, v61
	v_and_b32_e32 v13, 0xffff0000, v61
	v_fmac_f32_e32 v12, v10, v57
	v_fmac_f32_e32 v13, v11, v15
	v_lshlrev_b32_e32 v17, 16, v65
	v_and_b32_e32 v65, 0xffff0000, v65
	v_add_f32_e32 v170, v170, v12
	v_add_f32_e32 v171, v171, v13
	v_mul_f32_e32 v170, v170, v17
	v_mul_f32_e32 v171, v171, v65
	v_cvt_pk_bf16_f32 v65, v170, v171
	v_lshlrev_b32_e32 v10, 16, v60
	v_and_b32_e32 v11, 0xffff0000, v60
	v_fmac_f32_e32 v10, v12, v56
	v_fmac_f32_e32 v11, v13, v14
	v_lshlrev_b32_e32 v17, 16, v64
	v_and_b32_e32 v64, 0xffff0000, v64
	v_add_f32_e32 v168, v168, v10
	v_add_f32_e32 v169, v169, v11
	v_mul_f32_e32 v168, v168, v17
	v_mul_f32_e32 v169, v169, v64
	v_cvt_pk_bf16_f32 v64, v168, v169
	v_lshlrev_b32_e32 v12, 16, v59
	v_and_b32_e32 v13, 0xffff0000, v59
	v_fmac_f32_e32 v12, v10, v55
	v_fmac_f32_e32 v13, v11, v7
	v_lshlrev_b32_e32 v17, 16, v63
	v_and_b32_e32 v63, 0xffff0000, v63
	v_add_f32_e32 v166, v166, v12
	v_add_f32_e32 v167, v167, v13
	v_mul_f32_e32 v166, v166, v17
	v_mul_f32_e32 v167, v167, v63
	v_cvt_pk_bf16_f32 v63, v166, v167
	v_lshlrev_b32_e32 v10, 16, v58
	v_and_b32_e32 v11, 0xffff0000, v58
	v_fmac_f32_e32 v10, v12, v54
	v_fmac_f32_e32 v11, v13, v6
	v_lshlrev_b32_e32 v17, 16, v62
	v_and_b32_e32 v62, 0xffff0000, v62
	v_add_f32_e32 v164, v164, v10
	v_add_f32_e32 v165, v165, v11
	v_mul_f32_e32 v164, v164, v17
	v_mul_f32_e32 v165, v165, v62
	v_cvt_pk_bf16_f32 v62, v164, v165
	s_nop 1
	v_permlane16_swap_b32_e32 v62, v63
	v_permlane16_swap_b32_e32 v64, v65
	s_nop 1
	v_permlane32_swap_b32_e32 v62, v64
	v_permlane32_swap_b32_e32 v63, v65
	global_store_dwordx4 v5, v[62:65], s[80:81]
	v_add_u32_e32 v5, 0xffffe000, v5
	global_load_dwordx4 v[54:57], v4, s[82:83] nt
	global_load_dwordx4 v[58:61], v4, s[84:85] nt
	global_load_dwordx4 v[62:65], v4, s[78:79] nt
	v_add_u32_e32 v4, 0xffffe000, v4
	s_waitcnt vmcnt(12)
	v_permlane16_swap_b32_e32 v18, v19
	v_permlane16_swap_b32_e32 v20, v21
	v_permlane16_swap_b32_e32 v22, v23
	v_permlane16_swap_b32_e32 v24, v25
	v_permlane16_swap_b32_e32 v26, v27
	v_permlane16_swap_b32_e32 v28, v29
	v_permlane32_swap_b32_e32 v18, v20
	v_permlane32_swap_b32_e32 v19, v21
	v_permlane32_swap_b32_e32 v22, v24
	v_permlane32_swap_b32_e32 v23, v25
	v_permlane32_swap_b32_e32 v26, v28
	v_permlane32_swap_b32_e32 v27, v29
	v_and_b32_e32 v6, 0xffff0000, v18
	v_lshlrev_b32_e32 v18, 16, v18
	v_and_b32_e32 v7, 0xffff0000, v19
	v_lshlrev_b32_e32 v19, 16, v19
	v_and_b32_e32 v14, 0xffff0000, v20
	v_lshlrev_b32_e32 v20, 16, v20
	v_and_b32_e32 v15, 0xffff0000, v21
	v_lshlrev_b32_e32 v21, 16, v21
	v_mul_f32_e32 v18, 0x3fb8aa3b, v18
	v_mul_f32_e32 v6, 0x3fb8aa3b, v6
	v_mul_f32_e32 v19, 0x3fb8aa3b, v19
	v_mul_f32_e32 v7, 0x3fb8aa3b, v7
	v_mul_f32_e32 v20, 0x3fb8aa3b, v20
	v_mul_f32_e32 v14, 0x3fb8aa3b, v14
	v_mul_f32_e32 v21, 0x3fb8aa3b, v21
	v_mul_f32_e32 v15, 0x3fb8aa3b, v15
	v_exp_f32_e32 v18, v18
	v_exp_f32_e32 v6, v6
	v_exp_f32_e32 v19, v19
	v_exp_f32_e32 v7, v7
	v_exp_f32_e32 v20, v20
	v_exp_f32_e32 v14, v14
	v_exp_f32_e32 v21, v21
	v_exp_f32_e32 v15, v15
	v_lshlrev_b32_e32 v12, 16, v25
	v_and_b32_e32 v13, 0xffff0000, v25
	v_fmac_f32_e32 v12, v10, v21
	v_fmac_f32_e32 v13, v11, v15
	v_lshlrev_b32_e32 v17, 16, v29
	v_and_b32_e32 v29, 0xffff0000, v29
	v_add_f32_e32 v162, v162, v12
	v_add_f32_e32 v163, v163, v13
	v_mul_f32_e32 v162, v162, v17
	v_mul_f32_e32 v163, v163, v29
	v_cvt_pk_bf16_f32 v29, v162, v163
	v_lshlrev_b32_e32 v10, 16, v24
	v_and_b32_e32 v11, 0xffff0000, v24
	v_fmac_f32_e32 v10, v12, v20
	v_fmac_f32_e32 v11, v13, v14
	v_lshlrev_b32_e32 v17, 16, v28
	v_and_b32_e32 v28, 0xffff0000, v28
	v_add_f32_e32 v160, v160, v10
	v_add_f32_e32 v161, v161, v11
	v_mul_f32_e32 v160, v160, v17
	v_mul_f32_e32 v161, v161, v28
	v_cvt_pk_bf16_f32 v28, v160, v161
	v_lshlrev_b32_e32 v12, 16, v23
	v_and_b32_e32 v13, 0xffff0000, v23
	v_fmac_f32_e32 v12, v10, v19
	v_fmac_f32_e32 v13, v11, v7
	v_lshlrev_b32_e32 v17, 16, v27
	v_and_b32_e32 v27, 0xffff0000, v27
	v_add_f32_e32 v158, v158, v12
	v_add_f32_e32 v159, v159, v13
	v_mul_f32_e32 v158, v158, v17
	v_mul_f32_e32 v159, v159, v27
	v_cvt_pk_bf16_f32 v27, v158, v159
	v_lshlrev_b32_e32 v10, 16, v22
	v_and_b32_e32 v11, 0xffff0000, v22
	v_fmac_f32_e32 v10, v12, v18
	v_fmac_f32_e32 v11, v13, v6
	v_lshlrev_b32_e32 v17, 16, v26
	v_and_b32_e32 v26, 0xffff0000, v26
	v_add_f32_e32 v156, v156, v10
	v_add_f32_e32 v157, v157, v11
	v_mul_f32_e32 v156, v156, v17
	v_mul_f32_e32 v157, v157, v26
	v_cvt_pk_bf16_f32 v26, v156, v157
	s_nop 1
	v_permlane16_swap_b32_e32 v26, v27
	v_permlane16_swap_b32_e32 v28, v29
	s_nop 1
	v_permlane32_swap_b32_e32 v26, v28
	v_permlane32_swap_b32_e32 v27, v29
	global_store_dwordx4 v5, v[26:29], s[80:81]
	v_add_u32_e32 v5, 0xffffe000, v5
	global_load_dwordx4 v[18:21], v4, s[82:83] nt
	global_load_dwordx4 v[22:25], v4, s[84:85] nt
	global_load_dwordx4 v[26:29], v4, s[78:79] nt
	v_add_u32_e32 v4, 0xffffe000, v4
	s_waitcnt vmcnt(12)
; __device__ __forceinline__ unsigned cvt_pk_bf16(float lo, float hi) { unsigned r; asm("v_cvt_pk_bf16_f32 %0, %1, %2" : "=v"(r) : "v"(lo), "v"(hi)); return r; }
; __device__ __forceinline__ float bf_lo(unsigned w) { return __uint_as_float(w << 16); }
; __device__ __forceinline__ float bf_hi(unsigned w) { return __uint_as_float(w & 0xffff0000u); }
; __device__ __forceinline__ void scan_s3(CTXA) {
;     ...
;         for (int g = 0; g < 4; ++g) { unsigned wl[16], wb[16], wg[16];
; #pragma unroll
;             for (int q = 0; q < 16; ++q) { const int t = 63 - (g * 16 + q); wl[q] = __builtin_nontemporal_load(la1 + (size_t)t * (D / 2)); wb[q] = __builtin_nontemporal_load(bb1 + (size_t)t * (D / 2)); wg[q] = __builtin_nontemporal_load(gg + (size_t)t * (D / 2)); }
; #pragma unroll
;             for (int q = 0; q < 16; ++q) { const int t = 63 - (g * 16 + q); hb0 = __expf(bf_lo(wl[q])) * hb0 + bf_lo(wb[q]); hb1 = __expf(bf_hi(wl[q])) * hb1 + bf_hi(wb[q]);
;                 yy[(size_t)t * (D / 2)] = cvt_pk_bf16((fv0[t] + hb0) * bf_lo(wg[q]), (fv1[t] + hb1) * bf_hi(wg[q])); } }
	v_permlane16_swap_b32_e32 v30, v31
	v_permlane16_swap_b32_e32 v32, v33
	v_permlane16_swap_b32_e32 v34, v35
	v_permlane16_swap_b32_e32 v36, v37
	v_permlane16_swap_b32_e32 v38, v39
	v_permlane16_swap_b32_e32 v40, v41
	v_permlane32_swap_b32_e32 v30, v32
	v_permlane32_swap_b32_e32 v31, v33
	v_permlane32_swap_b32_e32 v34, v36
	v_permlane32_swap_b32_e32 v35, v37
	v_permlane32_swap_b32_e32 v38, v40
	v_permlane32_swap_b32_e32 v39, v41
	v_and_b32_e32 v6, 0xffff0000, v30
	v_lshlrev_b32_e32 v30, 16, v30
	v_and_b32_e32 v7, 0xffff0000, v31
	v_lshlrev_b32_e32 v31, 16, v31
	v_and_b32_e32 v14, 0xffff0000, v32
	v_lshlrev_b32_e32 v32, 16, v32
	v_and_b32_e32 v15, 0xffff0000, v33
	v_lshlrev_b32_e32 v33, 16, v33
	v_mul_f32_e32 v30, 0x3fb8aa3b, v30
	v_mul_f32_e32 v6, 0x3fb8aa3b, v6
	v_mul_f32_e32 v31, 0x3fb8aa3b, v31
	v_mul_f32_e32 v7, 0x3fb8aa3b, v7
	v_mul_f32_e32 v32, 0x3fb8aa3b, v32
	v_mul_f32_e32 v14, 0x3fb8aa3b, v14
	v_mul_f32_e32 v33, 0x3fb8aa3b, v33
	v_mul_f32_e32 v15, 0x3fb8aa3b, v15
	v_exp_f32_e32 v30, v30
	v_exp_f32_e32 v6, v6
	v_exp_f32_e32 v31, v31
	v_exp_f32_e32 v7, v7
	v_exp_f32_e32 v32, v32
	v_exp_f32_e32 v14, v14
	v_exp_f32_e32 v33, v33
	v_exp_f32_e32 v15, v15
	v_lshlrev_b32_e32 v12, 16, v37
	v_and_b32_e32 v13, 0xffff0000, v37
	v_fmac_f32_e32 v12, v10, v33
	v_fmac_f32_e32 v13, v11, v15
	v_lshlrev_b32_e32 v17, 16, v41
	v_and_b32_e32 v41, 0xffff0000, v41
	v_add_f32_e32 v154, v154, v12
	v_add_f32_e32 v155, v155, v13
	v_mul_f32_e32 v154, v154, v17
	v_mul_f32_e32 v155, v155, v41
	v_cvt_pk_bf16_f32 v41, v154, v155
	v_lshlrev_b32_e32 v10, 16, v36
	v_and_b32_e32 v11, 0xffff0000, v36
	v_fmac_f32_e32 v10, v12, v32
	v_fmac_f32_e32 v11, v13, v14
	v_lshlrev_b32_e32 v17, 16, v40
	v_and_b32_e32 v40, 0xffff0000, v40
	v_add_f32_e32 v152, v152, v10
	v_add_f32_e32 v153, v153, v11
	v_mul_f32_e32 v152, v152, v17
	v_mul_f32_e32 v153, v153, v40
	v_cvt_pk_bf16_f32 v40, v152, v153
	v_lshlrev_b32_e32 v12, 16, v35
	v_and_b32_e32 v13, 0xffff0000, v35
	v_fmac_f32_e32 v12, v10, v31
	v_fmac_f32_e32 v13, v11, v7
	v_lshlrev_b32_e32 v17, 16, v39
	v_and_b32_e32 v39, 0xffff0000, v39
	v_add_f32_e32 v150, v150, v12
	v_add_f32_e32 v151, v151, v13
	v_mul_f32_e32 v150, v150, v17
	v_mul_f32_e32 v151, v151, v39
	v_cvt_pk_bf16_f32 v39, v150, v151
	v_lshlrev_b32_e32 v10, 16, v34
	v_and_b32_e32 v11, 0xffff0000, v34
	v_fmac_f32_e32 v10, v12, v30
	v_fmac_f32_e32 v11, v13, v6
	v_lshlrev_b32_e32 v17, 16, v38
	v_and_b32_e32 v38, 0xffff0000, v38
	v_add_f32_e32 v148, v148, v10
	v_add_f32_e32 v149, v149, v11
	v_mul_f32_e32 v148, v148, v17
	v_mul_f32_e32 v149, v149, v38
	v_cvt_pk_bf16_f32 v38, v148, v149
	s_nop 1
	v_permlane16_swap_b32_e32 v38, v39
	v_permlane16_swap_b32_e32 v40, v41
	s_nop 1
	v_permlane32_swap_b32_e32 v38, v40
	v_permlane32_swap_b32_e32 v39, v41
	global_store_dwordx4 v5, v[38:41], s[80:81]
	v_add_u32_e32 v5, 0xffffe000, v5
	global_load_dwordx4 v[30:33], v4, s[82:83] nt
	global_load_dwordx4 v[34:37], v4, s[84:85] nt
	global_load_dwordx4 v[38:41], v4, s[78:79] nt
	v_add_u32_e32 v4, 0xffffe000, v4
	s_waitcnt vmcnt(12)
	v_permlane16_swap_b32_e32 v42, v43
	v_permlane16_swap_b32_e32 v44, v45
	v_permlane16_swap_b32_e32 v46, v47
	v_permlane16_swap_b32_e32 v48, v49
	v_permlane16_swap_b32_e32 v50, v51
	v_permlane16_swap_b32_e32 v52, v53
	v_permlane32_swap_b32_e32 v42, v44
	v_permlane32_swap_b32_e32 v43, v45
	v_permlane32_swap_b32_e32 v46, v48
	v_permlane32_swap_b32_e32 v47, v49
	v_permlane32_swap_b32_e32 v50, v52
	v_permlane32_swap_b32_e32 v51, v53
	v_and_b32_e32 v6, 0xffff0000, v42
	v_lshlrev_b32_e32 v42, 16, v42
	v_and_b32_e32 v7, 0xffff0000, v43
	v_lshlrev_b32_e32 v43, 16, v43
	v_and_b32_e32 v14, 0xffff0000, v44
	v_lshlrev_b32_e32 v44, 16, v44
	v_and_b32_e32 v15, 0xffff0000, v45
	v_lshlrev_b32_e32 v45, 16, v45
	v_mul_f32_e32 v42, 0x3fb8aa3b, v42
	v_mul_f32_e32 v6, 0x3fb8aa3b, v6
	v_mul_f32_e32 v43, 0x3fb8aa3b, v43
	v_mul_f32_e32 v7, 0x3fb8aa3b, v7
	v_mul_f32_e32 v44, 0x3fb8aa3b, v44
	v_mul_f32_e32 v14, 0x3fb8aa3b, v14
	v_mul_f32_e32 v45, 0x3fb8aa3b, v45
	v_mul_f32_e32 v15, 0x3fb8aa3b, v15
	v_exp_f32_e32 v42, v42
	v_exp_f32_e32 v6, v6
	v_exp_f32_e32 v43, v43
	v_exp_f32_e32 v7, v7
	v_exp_f32_e32 v44, v44
	v_exp_f32_e32 v14, v14
	v_exp_f32_e32 v45, v45
	v_exp_f32_e32 v15, v15
	v_lshlrev_b32_e32 v12, 16, v49
	v_and_b32_e32 v13, 0xffff0000, v49
	v_fmac_f32_e32 v12, v10, v45
	v_fmac_f32_e32 v13, v11, v15
	v_lshlrev_b32_e32 v17, 16, v53
	v_and_b32_e32 v53, 0xffff0000, v53
	v_add_f32_e32 v146, v146, v12
	v_add_f32_e32 v147, v147, v13
	v_mul_f32_e32 v146, v146, v17
	v_mul_f32_e32 v147, v147, v53
	v_cvt_pk_bf16_f32 v53, v146, v147
	v_lshlrev_b32_e32 v10, 16, v48
	v_and_b32_e32 v11, 0xffff0000, v48
	v_fmac_f32_e32 v10, v12, v44
	v_fmac_f32_e32 v11, v13, v14
	v_lshlrev_b32_e32 v17, 16, v52
	v_and_b32_e32 v52, 0xffff0000, v52
	v_add_f32_e32 v144, v144, v10
	v_add_f32_e32 v145, v145, v11
	v_mul_f32_e32 v144, v144, v17
	v_mul_f32_e32 v145, v145, v52
	v_cvt_pk_bf16_f32 v52, v144, v145
	v_lshlrev_b32_e32 v12, 16, v47
	v_and_b32_e32 v13, 0xffff0000, v47
	v_fmac_f32_e32 v12, v10, v43
	v_fmac_f32_e32 v13, v11, v7
	v_lshlrev_b32_e32 v17, 16, v51
	v_and_b32_e32 v51, 0xffff0000, v51
	v_add_f32_e32 v142, v142, v12
	v_add_f32_e32 v143, v143, v13
	v_mul_f32_e32 v142, v142, v17
	v_mul_f32_e32 v143, v143, v51
	v_cvt_pk_bf16_f32 v51, v142, v143
	v_lshlrev_b32_e32 v10, 16, v46
	v_and_b32_e32 v11, 0xffff0000, v46
	v_fmac_f32_e32 v10, v12, v42
	v_fmac_f32_e32 v11, v13, v6
	v_lshlrev_b32_e32 v17, 16, v50
	v_and_b32_e32 v50, 0xffff0000, v50
	v_add_f32_e32 v140, v140, v10
	v_add_f32_e32 v141, v141, v11
	v_mul_f32_e32 v140, v140, v17
	v_mul_f32_e32 v141, v141, v50
	v_cvt_pk_bf16_f32 v50, v140, v141
	s_nop 1
	v_permlane16_swap_b32_e32 v50, v51
	v_permlane16_swap_b32_e32 v52, v53
	s_nop 1
	v_permlane32_swap_b32_e32 v50, v52
	v_permlane32_swap_b32_e32 v51, v53
	global_store_dwordx4 v5, v[50:53], s[80:81]
	v_add_u32_e32 v5, 0xffffe000, v5
	global_load_dwordx4 v[42:45], v4, s[82:83] nt
	global_load_dwordx4 v[46:49], v4, s[84:85] nt
	global_load_dwordx4 v[50:53], v4, s[78:79] nt
	v_add_u32_e32 v4, 0xffffe000, v4
	s_waitcnt vmcnt(12)
; __device__ __forceinline__ unsigned cvt_pk_bf16(float lo, float hi) { unsigned r; asm("v_cvt_pk_bf16_f32 %0, %1, %2" : "=v"(r) : "v"(lo), "v"(hi)); return r; }
; __device__ __forceinline__ float bf_lo(unsigned w) { return __uint_as_float(w << 16); }
; __device__ __forceinline__ float bf_hi(unsigned w) { return __uint_as_float(w & 0xffff0000u); }
; __device__ __forceinline__ void scan_s3(CTXA) {
;     ...
;         for (int g = 0; g < 4; ++g) { unsigned wl[16], wb[16], wg[16];
; #pragma unroll
;             for (int q = 0; q < 16; ++q) { const int t = 63 - (g * 16 + q); wl[q] = __builtin_nontemporal_load(la1 + (size_t)t * (D / 2)); wb[q] = __builtin_nontemporal_load(bb1 + (size_t)t * (D / 2)); wg[q] = __builtin_nontemporal_load(gg + (size_t)t * (D / 2)); }
; #pragma unroll
;             for (int q = 0; q < 16; ++q) { const int t = 63 - (g * 16 + q); hb0 = __expf(bf_lo(wl[q])) * hb0 + bf_lo(wb[q]); hb1 = __expf(bf_hi(wl[q])) * hb1 + bf_hi(wb[q]);
;                 yy[(size_t)t * (D / 2)] = cvt_pk_bf16((fv0[t] + hb0) * bf_lo(wg[q]), (fv1[t] + hb1) * bf_hi(wg[q])); } }
	v_permlane16_swap_b32_e32 v54, v55
	v_permlane16_swap_b32_e32 v56, v57
	v_permlane16_swap_b32_e32 v58, v59
	v_permlane16_swap_b32_e32 v60, v61
	v_permlane16_swap_b32_e32 v62, v63
	v_permlane16_swap_b32_e32 v64, v65
	v_permlane32_swap_b32_e32 v54, v56
	v_permlane32_swap_b32_e32 v55, v57
	v_permlane32_swap_b32_e32 v58, v60
	v_permlane32_swap_b32_e32 v59, v61
	v_permlane32_swap_b32_e32 v62, v64
	v_permlane32_swap_b32_e32 v63, v65
	v_and_b32_e32 v6, 0xffff0000, v54
	v_lshlrev_b32_e32 v54, 16, v54
	v_and_b32_e32 v7, 0xffff0000, v55
	v_lshlrev_b32_e32 v55, 16, v55
	v_and_b32_e32 v14, 0xffff0000, v56
	v_lshlrev_b32_e32 v56, 16, v56
	v_and_b32_e32 v15, 0xffff0000, v57
	v_lshlrev_b32_e32 v57, 16, v57
	v_mul_f32_e32 v54, 0x3fb8aa3b, v54
	v_mul_f32_e32 v6, 0x3fb8aa3b, v6
	v_mul_f32_e32 v55, 0x3fb8aa3b, v55
	v_mul_f32_e32 v7, 0x3fb8aa3b, v7
	v_mul_f32_e32 v56, 0x3fb8aa3b, v56
	v_mul_f32_e32 v14, 0x3fb8aa3b, v14
	v_mul_f32_e32 v57, 0x3fb8aa3b, v57
	v_mul_f32_e32 v15, 0x3fb8aa3b, v15
	v_exp_f32_e32 v54, v54
	v_exp_f32_e32 v6, v6
	v_exp_f32_e32 v55, v55
	v_exp_f32_e32 v7, v7
	v_exp_f32_e32 v56, v56
	v_exp_f32_e32 v14, v14
	v_exp_f32_e32 v57, v57
	v_exp_f32_e32 v15, v15
	v_lshlrev_b32_e32 v12, 16, v61
	v_and_b32_e32 v13, 0xffff0000, v61
	v_fmac_f32_e32 v12, v10, v57
	v_fmac_f32_e32 v13, v11, v15
	v_lshlrev_b32_e32 v17, 16, v65
	v_and_b32_e32 v65, 0xffff0000, v65
	v_add_f32_e32 v138, v138, v12
	v_add_f32_e32 v139, v139, v13
	v_mul_f32_e32 v138, v138, v17
	v_mul_f32_e32 v139, v139, v65
	v_cvt_pk_bf16_f32 v65, v138, v139
	v_lshlrev_b32_e32 v10, 16, v60
	v_and_b32_e32 v11, 0xffff0000, v60
	v_fmac_f32_e32 v10, v12, v56
	v_fmac_f32_e32 v11, v13, v14
	v_lshlrev_b32_e32 v17, 16, v64
	v_and_b32_e32 v64, 0xffff0000, v64
	v_add_f32_e32 v136, v136, v10
	v_add_f32_e32 v137, v137, v11
	v_mul_f32_e32 v136, v136, v17
	v_mul_f32_e32 v137, v137, v64
	v_cvt_pk_bf16_f32 v64, v136, v137
	v_lshlrev_b32_e32 v12, 16, v59
	v_and_b32_e32 v13, 0xffff0000, v59
	v_fmac_f32_e32 v12, v10, v55
	v_fmac_f32_e32 v13, v11, v7
	v_lshlrev_b32_e32 v17, 16, v63
	v_and_b32_e32 v63, 0xffff0000, v63
	v_add_f32_e32 v134, v134, v12
	v_add_f32_e32 v135, v135, v13
	v_mul_f32_e32 v134, v134, v17
	v_mul_f32_e32 v135, v135, v63
	v_cvt_pk_bf16_f32 v63, v134, v135
	v_lshlrev_b32_e32 v10, 16, v58
	v_and_b32_e32 v11, 0xffff0000, v58
	v_fmac_f32_e32 v10, v12, v54
	v_fmac_f32_e32 v11, v13, v6
	v_lshlrev_b32_e32 v17, 16, v62
	v_and_b32_e32 v62, 0xffff0000, v62
	v_add_f32_e32 v132, v132, v10
	v_add_f32_e32 v133, v133, v11
	v_mul_f32_e32 v132, v132, v17
	v_mul_f32_e32 v133, v133, v62
	v_cvt_pk_bf16_f32 v62, v132, v133
	s_nop 1
	v_permlane16_swap_b32_e32 v62, v63
	v_permlane16_swap_b32_e32 v64, v65
	s_nop 1
	v_permlane32_swap_b32_e32 v62, v64
	v_permlane32_swap_b32_e32 v63, v65
	global_store_dwordx4 v5, v[62:65], s[80:81]
	v_add_u32_e32 v5, 0xffffe000, v5
	global_load_dwordx4 v[54:57], v4, s[82:83] nt
	global_load_dwordx4 v[58:61], v4, s[84:85] nt
	global_load_dwordx4 v[62:65], v4, s[78:79] nt
	v_add_u32_e32 v4, 0xffffe000, v4
	s_waitcnt vmcnt(12)
	v_permlane16_swap_b32_e32 v18, v19
	v_permlane16_swap_b32_e32 v20, v21
	v_permlane16_swap_b32_e32 v22, v23
	v_permlane16_swap_b32_e32 v24, v25
	v_permlane16_swap_b32_e32 v26, v27
	v_permlane16_swap_b32_e32 v28, v29
	v_permlane32_swap_b32_e32 v18, v20
	v_permlane32_swap_b32_e32 v19, v21
	v_permlane32_swap_b32_e32 v22, v24
	v_permlane32_swap_b32_e32 v23, v25
	v_permlane32_swap_b32_e32 v26, v28
	v_permlane32_swap_b32_e32 v27, v29
	v_and_b32_e32 v6, 0xffff0000, v18
	v_lshlrev_b32_e32 v18, 16, v18
	v_and_b32_e32 v7, 0xffff0000, v19
	v_lshlrev_b32_e32 v19, 16, v19
	v_and_b32_e32 v14, 0xffff0000, v20
	v_lshlrev_b32_e32 v20, 16, v20
	v_and_b32_e32 v15, 0xffff0000, v21
	v_lshlrev_b32_e32 v21, 16, v21
	v_mul_f32_e32 v18, 0x3fb8aa3b, v18
	v_mul_f32_e32 v6, 0x3fb8aa3b, v6
	v_mul_f32_e32 v19, 0x3fb8aa3b, v19
	v_mul_f32_e32 v7, 0x3fb8aa3b, v7
	v_mul_f32_e32 v20, 0x3fb8aa3b, v20
	v_mul_f32_e32 v14, 0x3fb8aa3b, v14
	v_mul_f32_e32 v21, 0x3fb8aa3b, v21
	v_mul_f32_e32 v15, 0x3fb8aa3b, v15
	v_exp_f32_e32 v18, v18
	v_exp_f32_e32 v6, v6
	v_exp_f32_e32 v19, v19
	v_exp_f32_e32 v7, v7
	v_exp_f32_e32 v20, v20
	v_exp_f32_e32 v14, v14
	v_exp_f32_e32 v21, v21
	v_exp_f32_e32 v15, v15
	v_lshlrev_b32_e32 v12, 16, v25
	v_and_b32_e32 v13, 0xffff0000, v25
	v_fmac_f32_e32 v12, v10, v21
	v_fmac_f32_e32 v13, v11, v15
	v_lshlrev_b32_e32 v17, 16, v29
	v_and_b32_e32 v29, 0xffff0000, v29
	v_add_f32_e32 v130, v130, v12
	v_add_f32_e32 v131, v131, v13
	v_mul_f32_e32 v130, v130, v17
	v_mul_f32_e32 v131, v131, v29
	v_cvt_pk_bf16_f32 v29, v130, v131
	v_lshlrev_b32_e32 v10, 16, v24
	v_and_b32_e32 v11, 0xffff0000, v24
	v_fmac_f32_e32 v10, v12, v20
	v_fmac_f32_e32 v11, v13, v14
	v_lshlrev_b32_e32 v17, 16, v28
	v_and_b32_e32 v28, 0xffff0000, v28
	v_add_f32_e32 v128, v128, v10
	v_add_f32_e32 v129, v129, v11
	v_mul_f32_e32 v128, v128, v17
	v_mul_f32_e32 v129, v129, v28
	v_cvt_pk_bf16_f32 v28, v128, v129
	v_lshlrev_b32_e32 v12, 16, v23
	v_and_b32_e32 v13, 0xffff0000, v23
	v_fmac_f32_e32 v12, v10, v19
	v_fmac_f32_e32 v13, v11, v7
	v_lshlrev_b32_e32 v17, 16, v27
	v_and_b32_e32 v27, 0xffff0000, v27
	v_add_f32_e32 v126, v126, v12
	v_add_f32_e32 v127, v127, v13
	v_mul_f32_e32 v126, v126, v17
	v_mul_f32_e32 v127, v127, v27
	v_cvt_pk_bf16_f32 v27, v126, v127
	v_lshlrev_b32_e32 v10, 16, v22
	v_and_b32_e32 v11, 0xffff0000, v22
	v_fmac_f32_e32 v10, v12, v18
	v_fmac_f32_e32 v11, v13, v6
	v_lshlrev_b32_e32 v17, 16, v26
	v_and_b32_e32 v26, 0xffff0000, v26
	v_add_f32_e32 v124, v124, v10
	v_add_f32_e32 v125, v125, v11
	v_mul_f32_e32 v124, v124, v17
	v_mul_f32_e32 v125, v125, v26
	v_cvt_pk_bf16_f32 v26, v124, v125
	s_nop 1
	v_permlane16_swap_b32_e32 v26, v27
	v_permlane16_swap_b32_e32 v28, v29
	s_nop 1
	v_permlane32_swap_b32_e32 v26, v28
	v_permlane32_swap_b32_e32 v27, v29
	global_store_dwordx4 v5, v[26:29], s[80:81]
	v_add_u32_e32 v5, 0xffffe000, v5
	global_load_dwordx4 v[18:21], v4, s[82:83] nt
	global_load_dwordx4 v[22:25], v4, s[84:85] nt
	global_load_dwordx4 v[26:29], v4, s[78:79] nt
	v_add_u32_e32 v4, 0xffffe000, v4
	s_waitcnt vmcnt(12)
; __device__ __forceinline__ unsigned cvt_pk_bf16(float lo, float hi) { unsigned r; asm("v_cvt_pk_bf16_f32 %0, %1, %2" : "=v"(r) : "v"(lo), "v"(hi)); return r; }
; __device__ __forceinline__ float bf_lo(unsigned w) { return __uint_as_float(w << 16); }
; __device__ __forceinline__ float bf_hi(unsigned w) { return __uint_as_float(w & 0xffff0000u); }
; __device__ __forceinline__ void scan_s3(CTXA) {
;     ...
;         for (int g = 0; g < 4; ++g) { unsigned wl[16], wb[16], wg[16];
; #pragma unroll
;             for (int q = 0; q < 16; ++q) { const int t = 63 - (g * 16 + q); wl[q] = __builtin_nontemporal_load(la1 + (size_t)t * (D / 2)); wb[q] = __builtin_nontemporal_load(bb1 + (size_t)t * (D / 2)); wg[q] = __builtin_nontemporal_load(gg + (size_t)t * (D / 2)); }
; #pragma unroll
;             for (int q = 0; q < 16; ++q) { const int t = 63 - (g * 16 + q); hb0 = __expf(bf_lo(wl[q])) * hb0 + bf_lo(wb[q]); hb1 = __expf(bf_hi(wl[q])) * hb1 + bf_hi(wb[q]);
;                 yy[(size_t)t * (D / 2)] = cvt_pk_bf16((fv0[t] + hb0) * bf_lo(wg[q]), (fv1[t] + hb1) * bf_hi(wg[q])); } }
	v_permlane16_swap_b32_e32 v30, v31
	v_permlane16_swap_b32_e32 v32, v33
	v_permlane16_swap_b32_e32 v34, v35
	v_permlane16_swap_b32_e32 v36, v37
	v_permlane16_swap_b32_e32 v38, v39
	v_permlane16_swap_b32_e32 v40, v41
	v_permlane32_swap_b32_e32 v30, v32
	v_permlane32_swap_b32_e32 v31, v33
	v_permlane32_swap_b32_e32 v34, v36
	v_permlane32_swap_b32_e32 v35, v37
	v_permlane32_swap_b32_e32 v38, v40
	v_permlane32_swap_b32_e32 v39, v41
	v_and_b32_e32 v6, 0xffff0000, v30
	v_lshlrev_b32_e32 v30, 16, v30
	v_and_b32_e32 v7, 0xffff0000, v31
	v_lshlrev_b32_e32 v31, 16, v31
	v_and_b32_e32 v14, 0xffff0000, v32
	v_lshlrev_b32_e32 v32, 16, v32
	v_and_b32_e32 v15, 0xffff0000, v33
	v_lshlrev_b32_e32 v33, 16, v33
	v_mul_f32_e32 v30, 0x3fb8aa3b, v30
	v_mul_f32_e32 v6, 0x3fb8aa3b, v6
	v_mul_f32_e32 v31, 0x3fb8aa3b, v31
	v_mul_f32_e32 v7, 0x3fb8aa3b, v7
	v_mul_f32_e32 v32, 0x3fb8aa3b, v32
	v_mul_f32_e32 v14, 0x3fb8aa3b, v14
	v_mul_f32_e32 v33, 0x3fb8aa3b, v33
	v_mul_f32_e32 v15, 0x3fb8aa3b, v15
	v_exp_f32_e32 v30, v30
	v_exp_f32_e32 v6, v6
	v_exp_f32_e32 v31, v31
	v_exp_f32_e32 v7, v7
	v_exp_f32_e32 v32, v32
	v_exp_f32_e32 v14, v14
	v_exp_f32_e32 v33, v33
	v_exp_f32_e32 v15, v15
	v_lshlrev_b32_e32 v12, 16, v37
	v_and_b32_e32 v13, 0xffff0000, v37
	v_fmac_f32_e32 v12, v10, v33
	v_fmac_f32_e32 v13, v11, v15
	v_lshlrev_b32_e32 v17, 16, v41
	v_and_b32_e32 v41, 0xffff0000, v41
	v_add_f32_e32 v122, v122, v12
	v_add_f32_e32 v123, v123, v13
	v_mul_f32_e32 v122, v122, v17
	v_mul_f32_e32 v123, v123, v41
	v_cvt_pk_bf16_f32 v41, v122, v123
	v_lshlrev_b32_e32 v10, 16, v36
	v_and_b32_e32 v11, 0xffff0000, v36
	v_fmac_f32_e32 v10, v12, v32
	v_fmac_f32_e32 v11, v13, v14
	v_lshlrev_b32_e32 v17, 16, v40
	v_and_b32_e32 v40, 0xffff0000, v40
	v_add_f32_e32 v120, v120, v10
	v_add_f32_e32 v121, v121, v11
	v_mul_f32_e32 v120, v120, v17
	v_mul_f32_e32 v121, v121, v40
	v_cvt_pk_bf16_f32 v40, v120, v121
	v_lshlrev_b32_e32 v12, 16, v35
	v_and_b32_e32 v13, 0xffff0000, v35
	v_fmac_f32_e32 v12, v10, v31
	v_fmac_f32_e32 v13, v11, v7
	v_lshlrev_b32_e32 v17, 16, v39
	v_and_b32_e32 v39, 0xffff0000, v39
	v_add_f32_e32 v118, v118, v12
	v_add_f32_e32 v119, v119, v13
	v_mul_f32_e32 v118, v118, v17
	v_mul_f32_e32 v119, v119, v39
	v_cvt_pk_bf16_f32 v39, v118, v119
	v_lshlrev_b32_e32 v10, 16, v34
	v_and_b32_e32 v11, 0xffff0000, v34
	v_fmac_f32_e32 v10, v12, v30
	v_fmac_f32_e32 v11, v13, v6
	v_lshlrev_b32_e32 v17, 16, v38
	v_and_b32_e32 v38, 0xffff0000, v38
	v_add_f32_e32 v116, v116, v10
	v_add_f32_e32 v117, v117, v11
	v_mul_f32_e32 v116, v116, v17
	v_mul_f32_e32 v117, v117, v38
	v_cvt_pk_bf16_f32 v38, v116, v117
	s_nop 1
	v_permlane16_swap_b32_e32 v38, v39
	v_permlane16_swap_b32_e32 v40, v41
	s_nop 1
	v_permlane32_swap_b32_e32 v38, v40
	v_permlane32_swap_b32_e32 v39, v41
	global_store_dwordx4 v5, v[38:41], s[80:81]
	v_add_u32_e32 v5, 0xffffe000, v5
	global_load_dwordx4 v[30:33], v4, s[82:83] nt
	global_load_dwordx4 v[34:37], v4, s[84:85] nt
	global_load_dwordx4 v[38:41], v4, s[78:79] nt
	v_add_u32_e32 v4, 0xffffe000, v4
	s_waitcnt vmcnt(12)
	v_permlane16_swap_b32_e32 v42, v43
	v_permlane16_swap_b32_e32 v44, v45
	v_permlane16_swap_b32_e32 v46, v47
	v_permlane16_swap_b32_e32 v48, v49
	v_permlane16_swap_b32_e32 v50, v51
	v_permlane16_swap_b32_e32 v52, v53
	v_permlane32_swap_b32_e32 v42, v44
	v_permlane32_swap_b32_e32 v43, v45
	v_permlane32_swap_b32_e32 v46, v48
	v_permlane32_swap_b32_e32 v47, v49
	v_permlane32_swap_b32_e32 v50, v52
	v_permlane32_swap_b32_e32 v51, v53
	v_and_b32_e32 v6, 0xffff0000, v42
	v_lshlrev_b32_e32 v42, 16, v42
	v_and_b32_e32 v7, 0xffff0000, v43
	v_lshlrev_b32_e32 v43, 16, v43
	v_and_b32_e32 v14, 0xffff0000, v44
	v_lshlrev_b32_e32 v44, 16, v44
	v_and_b32_e32 v15, 0xffff0000, v45
	v_lshlrev_b32_e32 v45, 16, v45
	v_mul_f32_e32 v42, 0x3fb8aa3b, v42
	v_mul_f32_e32 v6, 0x3fb8aa3b, v6
	v_mul_f32_e32 v43, 0x3fb8aa3b, v43
	v_mul_f32_e32 v7, 0x3fb8aa3b, v7
	v_mul_f32_e32 v44, 0x3fb8aa3b, v44
	v_mul_f32_e32 v14, 0x3fb8aa3b, v14
	v_mul_f32_e32 v45, 0x3fb8aa3b, v45
	v_mul_f32_e32 v15, 0x3fb8aa3b, v15
	v_exp_f32_e32 v42, v42
	v_exp_f32_e32 v6, v6
	v_exp_f32_e32 v43, v43
	v_exp_f32_e32 v7, v7
	v_exp_f32_e32 v44, v44
	v_exp_f32_e32 v14, v14
	v_exp_f32_e32 v45, v45
	v_exp_f32_e32 v15, v15
	v_lshlrev_b32_e32 v12, 16, v49
	v_and_b32_e32 v13, 0xffff0000, v49
	v_fmac_f32_e32 v12, v10, v45
	v_fmac_f32_e32 v13, v11, v15
	v_lshlrev_b32_e32 v17, 16, v53
	v_and_b32_e32 v53, 0xffff0000, v53
	v_add_f32_e32 v114, v114, v12
	v_add_f32_e32 v115, v115, v13
	v_mul_f32_e32 v114, v114, v17
	v_mul_f32_e32 v115, v115, v53
	v_cvt_pk_bf16_f32 v53, v114, v115
	v_lshlrev_b32_e32 v10, 16, v48
	v_and_b32_e32 v11, 0xffff0000, v48
	v_fmac_f32_e32 v10, v12, v44
	v_fmac_f32_e32 v11, v13, v14
	v_lshlrev_b32_e32 v17, 16, v52
	v_and_b32_e32 v52, 0xffff0000, v52
	v_add_f32_e32 v112, v112, v10
	v_add_f32_e32 v113, v113, v11
	v_mul_f32_e32 v112, v112, v17
	v_mul_f32_e32 v113, v113, v52
	v_cvt_pk_bf16_f32 v52, v112, v113
	v_lshlrev_b32_e32 v12, 16, v47
	v_and_b32_e32 v13, 0xffff0000, v47
	v_fmac_f32_e32 v12, v10, v43
	v_fmac_f32_e32 v13, v11, v7
	v_lshlrev_b32_e32 v17, 16, v51
	v_and_b32_e32 v51, 0xffff0000, v51
	v_add_f32_e32 v110, v110, v12
	v_add_f32_e32 v111, v111, v13
	v_mul_f32_e32 v110, v110, v17
	v_mul_f32_e32 v111, v111, v51
	v_cvt_pk_bf16_f32 v51, v110, v111
	v_lshlrev_b32_e32 v10, 16, v46
	v_and_b32_e32 v11, 0xffff0000, v46
	v_fmac_f32_e32 v10, v12, v42
	v_fmac_f32_e32 v11, v13, v6
	v_lshlrev_b32_e32 v17, 16, v50
	v_and_b32_e32 v50, 0xffff0000, v50
	v_add_f32_e32 v108, v108, v10
	v_add_f32_e32 v109, v109, v11
	v_mul_f32_e32 v108, v108, v17
	v_mul_f32_e32 v109, v109, v50
	v_cvt_pk_bf16_f32 v50, v108, v109
	s_nop 1
	v_permlane16_swap_b32_e32 v50, v51
	v_permlane16_swap_b32_e32 v52, v53
	s_nop 1
	v_permlane32_swap_b32_e32 v50, v52
	v_permlane32_swap_b32_e32 v51, v53
	global_store_dwordx4 v5, v[50:53], s[80:81]
	v_add_u32_e32 v5, 0xffffe000, v5
	global_load_dwordx4 v[42:45], v4, s[82:83] nt
	global_load_dwordx4 v[46:49], v4, s[84:85] nt
	global_load_dwordx4 v[50:53], v4, s[78:79] nt
	v_add_u32_e32 v4, 0xffffe000, v4
	s_waitcnt vmcnt(12)
; __device__ __forceinline__ unsigned cvt_pk_bf16(float lo, float hi) { unsigned r; asm("v_cvt_pk_bf16_f32 %0, %1, %2" : "=v"(r) : "v"(lo), "v"(hi)); return r; }
; __device__ __forceinline__ float bf_lo(unsigned w) { return __uint_as_float(w << 16); }
; __device__ __forceinline__ float bf_hi(unsigned w) { return __uint_as_float(w & 0xffff0000u); }
; __device__ __forceinline__ void scan_s3(CTXA) {
;     ...
;         for (int g = 0; g < 4; ++g) { unsigned wl[16], wb[16], wg[16];
; #pragma unroll
;             for (int q = 0; q < 16; ++q) { const int t = 63 - (g * 16 + q); wl[q] = __builtin_nontemporal_load(la1 + (size_t)t * (D / 2)); wb[q] = __builtin_nontemporal_load(bb1 + (size_t)t * (D / 2)); wg[q] = __builtin_nontemporal_load(gg + (size_t)t * (D / 2)); }
; #pragma unroll
;             for (int q = 0; q < 16; ++q) { const int t = 63 - (g * 16 + q); hb0 = __expf(bf_lo(wl[q])) * hb0 + bf_lo(wb[q]); hb1 = __expf(bf_hi(wl[q])) * hb1 + bf_hi(wb[q]);
;                 yy[(size_t)t * (D / 2)] = cvt_pk_bf16((fv0[t] + hb0) * bf_lo(wg[q]), (fv1[t] + hb1) * bf_hi(wg[q])); } }
	v_permlane16_swap_b32_e32 v54, v55
	v_permlane16_swap_b32_e32 v56, v57
	v_permlane16_swap_b32_e32 v58, v59
	v_permlane16_swap_b32_e32 v60, v61
	v_permlane16_swap_b32_e32 v62, v63
	v_permlane16_swap_b32_e32 v64, v65
	v_permlane32_swap_b32_e32 v54, v56
	v_permlane32_swap_b32_e32 v55, v57
	v_permlane32_swap_b32_e32 v58, v60
	v_permlane32_swap_b32_e32 v59, v61
	v_permlane32_swap_b32_e32 v62, v64
	v_permlane32_swap_b32_e32 v63, v65
	v_and_b32_e32 v6, 0xffff0000, v54
	v_lshlrev_b32_e32 v54, 16, v54
	v_and_b32_e32 v7, 0xffff0000, v55
	v_lshlrev_b32_e32 v55, 16, v55
	v_and_b32_e32 v14, 0xffff0000, v56
	v_lshlrev_b32_e32 v56, 16, v56
	v_and_b32_e32 v15, 0xffff0000, v57
	v_lshlrev_b32_e32 v57, 16, v57
	v_mul_f32_e32 v54, 0x3fb8aa3b, v54
	v_mul_f32_e32 v6, 0x3fb8aa3b, v6
	v_mul_f32_e32 v55, 0x3fb8aa3b, v55
	v_mul_f32_e32 v7, 0x3fb8aa3b, v7
	v_mul_f32_e32 v56, 0x3fb8aa3b, v56
	v_mul_f32_e32 v14, 0x3fb8aa3b, v14
	v_mul_f32_e32 v57, 0x3fb8aa3b, v57
	v_mul_f32_e32 v15, 0x3fb8aa3b, v15
	v_exp_f32_e32 v54, v54
	v_exp_f32_e32 v6, v6
	v_exp_f32_e32 v55, v55
	v_exp_f32_e32 v7, v7
	v_exp_f32_e32 v56, v56
	v_exp_f32_e32 v14, v14
	v_exp_f32_e32 v57, v57
	v_exp_f32_e32 v15, v15
	v_lshlrev_b32_e32 v12, 16, v61
	v_and_b32_e32 v13, 0xffff0000, v61
	v_fmac_f32_e32 v12, v10, v57
	v_fmac_f32_e32 v13, v11, v15
	v_lshlrev_b32_e32 v17, 16, v65
	v_and_b32_e32 v65, 0xffff0000, v65
	v_add_f32_e32 v106, v106, v12
	v_add_f32_e32 v107, v107, v13
	v_mul_f32_e32 v106, v106, v17
	v_mul_f32_e32 v107, v107, v65
	v_cvt_pk_bf16_f32 v65, v106, v107
	v_lshlrev_b32_e32 v10, 16, v60
	v_and_b32_e32 v11, 0xffff0000, v60
	v_fmac_f32_e32 v10, v12, v56
	v_fmac_f32_e32 v11, v13, v14
	v_lshlrev_b32_e32 v17, 16, v64
	v_and_b32_e32 v64, 0xffff0000, v64
	v_add_f32_e32 v104, v104, v10
	v_add_f32_e32 v105, v105, v11
	v_mul_f32_e32 v104, v104, v17
	v_mul_f32_e32 v105, v105, v64
	v_cvt_pk_bf16_f32 v64, v104, v105
	v_lshlrev_b32_e32 v12, 16, v59
	v_and_b32_e32 v13, 0xffff0000, v59
	v_fmac_f32_e32 v12, v10, v55
	v_fmac_f32_e32 v13, v11, v7
	v_lshlrev_b32_e32 v17, 16, v63
	v_and_b32_e32 v63, 0xffff0000, v63
	v_add_f32_e32 v102, v102, v12
	v_add_f32_e32 v103, v103, v13
	v_mul_f32_e32 v102, v102, v17
	v_mul_f32_e32 v103, v103, v63
	v_cvt_pk_bf16_f32 v63, v102, v103
	v_lshlrev_b32_e32 v10, 16, v58
	v_and_b32_e32 v11, 0xffff0000, v58
	v_fmac_f32_e32 v10, v12, v54
	v_fmac_f32_e32 v11, v13, v6
	v_lshlrev_b32_e32 v17, 16, v62
	v_and_b32_e32 v62, 0xffff0000, v62
	v_add_f32_e32 v100, v100, v10
	v_add_f32_e32 v101, v101, v11
	v_mul_f32_e32 v100, v100, v17
	v_mul_f32_e32 v101, v101, v62
	v_cvt_pk_bf16_f32 v62, v100, v101
	s_nop 1
	v_permlane16_swap_b32_e32 v62, v63
	v_permlane16_swap_b32_e32 v64, v65
	s_nop 1
	v_permlane32_swap_b32_e32 v62, v64
	v_permlane32_swap_b32_e32 v63, v65
	global_store_dwordx4 v5, v[62:65], s[80:81]
	v_add_u32_e32 v5, 0xffffe000, v5
	global_load_dwordx4 v[54:57], v4, s[82:83] nt
	global_load_dwordx4 v[58:61], v4, s[84:85] nt
	global_load_dwordx4 v[62:65], v4, s[78:79] nt
	s_waitcnt vmcnt(12)
	v_permlane16_swap_b32_e32 v18, v19
	v_permlane16_swap_b32_e32 v20, v21
	v_permlane16_swap_b32_e32 v22, v23
	v_permlane16_swap_b32_e32 v24, v25
	v_permlane16_swap_b32_e32 v26, v27
	v_permlane16_swap_b32_e32 v28, v29
	v_permlane32_swap_b32_e32 v18, v20
	v_permlane32_swap_b32_e32 v19, v21
	v_permlane32_swap_b32_e32 v22, v24
	v_permlane32_swap_b32_e32 v23, v25
	v_permlane32_swap_b32_e32 v26, v28
	v_permlane32_swap_b32_e32 v27, v29
	v_and_b32_e32 v6, 0xffff0000, v18
	v_lshlrev_b32_e32 v18, 16, v18
	v_and_b32_e32 v7, 0xffff0000, v19
	v_lshlrev_b32_e32 v19, 16, v19
	v_and_b32_e32 v14, 0xffff0000, v20
	v_lshlrev_b32_e32 v20, 16, v20
	v_and_b32_e32 v15, 0xffff0000, v21
	v_lshlrev_b32_e32 v21, 16, v21
	v_mul_f32_e32 v18, 0x3fb8aa3b, v18
	v_mul_f32_e32 v6, 0x3fb8aa3b, v6
	v_mul_f32_e32 v19, 0x3fb8aa3b, v19
	v_mul_f32_e32 v7, 0x3fb8aa3b, v7
	v_mul_f32_e32 v20, 0x3fb8aa3b, v20
	v_mul_f32_e32 v14, 0x3fb8aa3b, v14
	v_mul_f32_e32 v21, 0x3fb8aa3b, v21
	v_mul_f32_e32 v15, 0x3fb8aa3b, v15
	v_exp_f32_e32 v18, v18
	v_exp_f32_e32 v6, v6
	v_exp_f32_e32 v19, v19
	v_exp_f32_e32 v7, v7
	v_exp_f32_e32 v20, v20
	v_exp_f32_e32 v14, v14
	v_exp_f32_e32 v21, v21
	v_exp_f32_e32 v15, v15
	v_lshlrev_b32_e32 v12, 16, v25
	v_and_b32_e32 v13, 0xffff0000, v25
	v_fmac_f32_e32 v12, v10, v21
	v_fmac_f32_e32 v13, v11, v15
	v_lshlrev_b32_e32 v17, 16, v29
	v_and_b32_e32 v29, 0xffff0000, v29
	v_add_f32_e32 v98, v98, v12
	v_add_f32_e32 v99, v99, v13
	v_mul_f32_e32 v98, v98, v17
	v_mul_f32_e32 v99, v99, v29
	v_cvt_pk_bf16_f32 v29, v98, v99
	v_lshlrev_b32_e32 v10, 16, v24
	v_and_b32_e32 v11, 0xffff0000, v24
	v_fmac_f32_e32 v10, v12, v20
	v_fmac_f32_e32 v11, v13, v14
	v_lshlrev_b32_e32 v17, 16, v28
	v_and_b32_e32 v28, 0xffff0000, v28
	v_add_f32_e32 v96, v96, v10
	v_add_f32_e32 v97, v97, v11
	v_mul_f32_e32 v96, v96, v17
	v_mul_f32_e32 v97, v97, v28
	v_cvt_pk_bf16_f32 v28, v96, v97
	v_lshlrev_b32_e32 v12, 16, v23
	v_and_b32_e32 v13, 0xffff0000, v23
	v_fmac_f32_e32 v12, v10, v19
	v_fmac_f32_e32 v13, v11, v7
	v_lshlrev_b32_e32 v17, 16, v27
	v_and_b32_e32 v27, 0xffff0000, v27
	v_add_f32_e32 v94, v94, v12
	v_add_f32_e32 v95, v95, v13
	v_mul_f32_e32 v94, v94, v17
	v_mul_f32_e32 v95, v95, v27
	v_cvt_pk_bf16_f32 v27, v94, v95
	v_lshlrev_b32_e32 v10, 16, v22
	v_and_b32_e32 v11, 0xffff0000, v22
	v_fmac_f32_e32 v10, v12, v18
	v_fmac_f32_e32 v11, v13, v6
	v_lshlrev_b32_e32 v17, 16, v26
	v_and_b32_e32 v26, 0xffff0000, v26
	v_add_f32_e32 v92, v92, v10
	v_add_f32_e32 v93, v93, v11
	v_mul_f32_e32 v92, v92, v17
	v_mul_f32_e32 v93, v93, v26
	v_cvt_pk_bf16_f32 v26, v92, v93
	s_nop 1
	v_permlane16_swap_b32_e32 v26, v27
	v_permlane16_swap_b32_e32 v28, v29
	s_nop 1
	v_permlane32_swap_b32_e32 v26, v28
	v_permlane32_swap_b32_e32 v27, v29
	global_store_dwordx4 v5, v[26:29], s[80:81]
	v_add_u32_e32 v5, 0xffffe000, v5
	s_waitcnt vmcnt(9)
; __device__ __forceinline__ unsigned cvt_pk_bf16(float lo, float hi) { unsigned r; asm("v_cvt_pk_bf16_f32 %0, %1, %2" : "=v"(r) : "v"(lo), "v"(hi)); return r; }
; __device__ __forceinline__ float bf_lo(unsigned w) { return __uint_as_float(w << 16); }
; __device__ __forceinline__ float bf_hi(unsigned w) { return __uint_as_float(w & 0xffff0000u); }
; __device__ __forceinline__ void scan_s3(CTXA) {
;     ...
;         for (int g = 0; g < 4; ++g) { unsigned wl[16], wb[16], wg[16];
; #pragma unroll
;             for (int q = 0; q < 16; ++q) { const int t = 63 - (g * 16 + q); wl[q] = __builtin_nontemporal_load(la1 + (size_t)t * (D / 2)); wb[q] = __builtin_nontemporal_load(bb1 + (size_t)t * (D / 2)); wg[q] = __builtin_nontemporal_load(gg + (size_t)t * (D / 2)); }
; #pragma unroll
;             for (int q = 0; q < 16; ++q) { const int t = 63 - (g * 16 + q); hb0 = __expf(bf_lo(wl[q])) * hb0 + bf_lo(wb[q]); hb1 = __expf(bf_hi(wl[q])) * hb1 + bf_hi(wb[q]);
;                 yy[(size_t)t * (D / 2)] = cvt_pk_bf16((fv0[t] + hb0) * bf_lo(wg[q]), (fv1[t] + hb1) * bf_hi(wg[q])); } }
	v_permlane16_swap_b32_e32 v30, v31
	v_permlane16_swap_b32_e32 v32, v33
	v_permlane16_swap_b32_e32 v34, v35
	v_permlane16_swap_b32_e32 v36, v37
	v_permlane16_swap_b32_e32 v38, v39
	v_permlane16_swap_b32_e32 v40, v41
	v_permlane32_swap_b32_e32 v30, v32
	v_permlane32_swap_b32_e32 v31, v33
	v_permlane32_swap_b32_e32 v34, v36
	v_permlane32_swap_b32_e32 v35, v37
	v_permlane32_swap_b32_e32 v38, v40
	v_permlane32_swap_b32_e32 v39, v41
	v_and_b32_e32 v6, 0xffff0000, v30
	v_lshlrev_b32_e32 v30, 16, v30
	v_and_b32_e32 v7, 0xffff0000, v31
	v_lshlrev_b32_e32 v31, 16, v31
	v_and_b32_e32 v14, 0xffff0000, v32
	v_lshlrev_b32_e32 v32, 16, v32
	v_and_b32_e32 v15, 0xffff0000, v33
	v_lshlrev_b32_e32 v33, 16, v33
	v_mul_f32_e32 v30, 0x3fb8aa3b, v30
	v_mul_f32_e32 v6, 0x3fb8aa3b, v6
	v_mul_f32_e32 v31, 0x3fb8aa3b, v31
	v_mul_f32_e32 v7, 0x3fb8aa3b, v7
	v_mul_f32_e32 v32, 0x3fb8aa3b, v32
	v_mul_f32_e32 v14, 0x3fb8aa3b, v14
	v_mul_f32_e32 v33, 0x3fb8aa3b, v33
	v_mul_f32_e32 v15, 0x3fb8aa3b, v15
	v_exp_f32_e32 v30, v30
	v_exp_f32_e32 v6, v6
	v_exp_f32_e32 v31, v31
	v_exp_f32_e32 v7, v7
	v_exp_f32_e32 v32, v32
	v_exp_f32_e32 v14, v14
	v_exp_f32_e32 v33, v33
	v_exp_f32_e32 v15, v15
	v_lshlrev_b32_e32 v12, 16, v37
	v_and_b32_e32 v13, 0xffff0000, v37
	v_fmac_f32_e32 v12, v10, v33
	v_fmac_f32_e32 v13, v11, v15
	v_lshlrev_b32_e32 v17, 16, v41
	v_and_b32_e32 v41, 0xffff0000, v41
	v_add_f32_e32 v90, v90, v12
	v_add_f32_e32 v91, v91, v13
	v_mul_f32_e32 v90, v90, v17
	v_mul_f32_e32 v91, v91, v41
	v_cvt_pk_bf16_f32 v41, v90, v91
	v_lshlrev_b32_e32 v10, 16, v36
	v_and_b32_e32 v11, 0xffff0000, v36
	v_fmac_f32_e32 v10, v12, v32
	v_fmac_f32_e32 v11, v13, v14
	v_lshlrev_b32_e32 v17, 16, v40
	v_and_b32_e32 v40, 0xffff0000, v40
	v_add_f32_e32 v88, v88, v10
	v_add_f32_e32 v89, v89, v11
	v_mul_f32_e32 v88, v88, v17
	v_mul_f32_e32 v89, v89, v40
	v_cvt_pk_bf16_f32 v40, v88, v89
	v_lshlrev_b32_e32 v12, 16, v35
	v_and_b32_e32 v13, 0xffff0000, v35
	v_fmac_f32_e32 v12, v10, v31
	v_fmac_f32_e32 v13, v11, v7
	v_lshlrev_b32_e32 v17, 16, v39
	v_and_b32_e32 v39, 0xffff0000, v39
	v_add_f32_e32 v86, v86, v12
	v_add_f32_e32 v87, v87, v13
	v_mul_f32_e32 v86, v86, v17
	v_mul_f32_e32 v87, v87, v39
	v_cvt_pk_bf16_f32 v39, v86, v87
	v_lshlrev_b32_e32 v10, 16, v34
	v_and_b32_e32 v11, 0xffff0000, v34
	v_fmac_f32_e32 v10, v12, v30
	v_fmac_f32_e32 v11, v13, v6
	v_lshlrev_b32_e32 v17, 16, v38
	v_and_b32_e32 v38, 0xffff0000, v38
	v_add_f32_e32 v84, v84, v10
	v_add_f32_e32 v85, v85, v11
	v_mul_f32_e32 v84, v84, v17
	v_mul_f32_e32 v85, v85, v38
	v_cvt_pk_bf16_f32 v38, v84, v85
	s_nop 1
	v_permlane16_swap_b32_e32 v38, v39
	v_permlane16_swap_b32_e32 v40, v41
	s_nop 1
	v_permlane32_swap_b32_e32 v38, v40
	v_permlane32_swap_b32_e32 v39, v41
	global_store_dwordx4 v5, v[38:41], s[80:81]
	v_add_u32_e32 v5, 0xffffe000, v5
	s_waitcnt vmcnt(6)
	v_permlane16_swap_b32_e32 v42, v43
	v_permlane16_swap_b32_e32 v44, v45
	v_permlane16_swap_b32_e32 v46, v47
	v_permlane16_swap_b32_e32 v48, v49
	v_permlane16_swap_b32_e32 v50, v51
	v_permlane16_swap_b32_e32 v52, v53
	v_permlane32_swap_b32_e32 v42, v44
	v_permlane32_swap_b32_e32 v43, v45
	v_permlane32_swap_b32_e32 v46, v48
	v_permlane32_swap_b32_e32 v47, v49
	v_permlane32_swap_b32_e32 v50, v52
	v_permlane32_swap_b32_e32 v51, v53
	v_and_b32_e32 v6, 0xffff0000, v42
	v_lshlrev_b32_e32 v42, 16, v42
	v_and_b32_e32 v7, 0xffff0000, v43
	v_lshlrev_b32_e32 v43, 16, v43
	v_and_b32_e32 v14, 0xffff0000, v44
	v_lshlrev_b32_e32 v44, 16, v44
	v_and_b32_e32 v15, 0xffff0000, v45
	v_lshlrev_b32_e32 v45, 16, v45
	v_mul_f32_e32 v42, 0x3fb8aa3b, v42
	v_mul_f32_e32 v6, 0x3fb8aa3b, v6
	v_mul_f32_e32 v43, 0x3fb8aa3b, v43
	v_mul_f32_e32 v7, 0x3fb8aa3b, v7
	v_mul_f32_e32 v44, 0x3fb8aa3b, v44
	v_mul_f32_e32 v14, 0x3fb8aa3b, v14
	v_mul_f32_e32 v45, 0x3fb8aa3b, v45
	v_mul_f32_e32 v15, 0x3fb8aa3b, v15
	v_exp_f32_e32 v42, v42
	v_exp_f32_e32 v6, v6
	v_exp_f32_e32 v43, v43
	v_exp_f32_e32 v7, v7
	v_exp_f32_e32 v44, v44
	v_exp_f32_e32 v14, v14
	v_exp_f32_e32 v45, v45
	v_exp_f32_e32 v15, v15
	v_lshlrev_b32_e32 v12, 16, v49
	v_and_b32_e32 v13, 0xffff0000, v49
	v_fmac_f32_e32 v12, v10, v45
	v_fmac_f32_e32 v13, v11, v15
	v_lshlrev_b32_e32 v17, 16, v53
	v_and_b32_e32 v53, 0xffff0000, v53
	v_add_f32_e32 v82, v82, v12
	v_add_f32_e32 v83, v83, v13
	v_mul_f32_e32 v82, v82, v17
	v_mul_f32_e32 v83, v83, v53
	v_cvt_pk_bf16_f32 v53, v82, v83
	v_lshlrev_b32_e32 v10, 16, v48
	v_and_b32_e32 v11, 0xffff0000, v48
	v_fmac_f32_e32 v10, v12, v44
	v_fmac_f32_e32 v11, v13, v14
	v_lshlrev_b32_e32 v17, 16, v52
	v_and_b32_e32 v52, 0xffff0000, v52
	v_add_f32_e32 v80, v80, v10
	v_add_f32_e32 v81, v81, v11
	v_mul_f32_e32 v80, v80, v17
	v_mul_f32_e32 v81, v81, v52
	v_cvt_pk_bf16_f32 v52, v80, v81
	v_lshlrev_b32_e32 v12, 16, v47
	v_and_b32_e32 v13, 0xffff0000, v47
	v_fmac_f32_e32 v12, v10, v43
	v_fmac_f32_e32 v13, v11, v7
	v_lshlrev_b32_e32 v17, 16, v51
	v_and_b32_e32 v51, 0xffff0000, v51
	v_add_f32_e32 v78, v78, v12
	v_add_f32_e32 v79, v79, v13
	v_mul_f32_e32 v78, v78, v17
	v_mul_f32_e32 v79, v79, v51
	v_cvt_pk_bf16_f32 v51, v78, v79
	v_lshlrev_b32_e32 v10, 16, v46
	v_and_b32_e32 v11, 0xffff0000, v46
	v_fmac_f32_e32 v10, v12, v42
	v_fmac_f32_e32 v11, v13, v6
	v_lshlrev_b32_e32 v17, 16, v50
	v_and_b32_e32 v50, 0xffff0000, v50
	v_add_f32_e32 v76, v76, v10
	v_add_f32_e32 v77, v77, v11
	v_mul_f32_e32 v76, v76, v17
	v_mul_f32_e32 v77, v77, v50
	v_cvt_pk_bf16_f32 v50, v76, v77
	s_nop 1
	v_permlane16_swap_b32_e32 v50, v51
	v_permlane16_swap_b32_e32 v52, v53
	s_nop 1
	v_permlane32_swap_b32_e32 v50, v52
	v_permlane32_swap_b32_e32 v51, v53
	global_store_dwordx4 v5, v[50:53], s[80:81]
	v_add_u32_e32 v5, 0xffffe000, v5
	s_waitcnt vmcnt(3)
; __device__ __forceinline__ unsigned cvt_pk_bf16(float lo, float hi) { unsigned r; asm("v_cvt_pk_bf16_f32 %0, %1, %2" : "=v"(r) : "v"(lo), "v"(hi)); return r; }
; __device__ __forceinline__ float bf_lo(unsigned w) { return __uint_as_float(w << 16); }
; __device__ __forceinline__ float bf_hi(unsigned w) { return __uint_as_float(w & 0xffff0000u); }
; __device__ __forceinline__ void scan_s3(CTXA) {
;     ...
;     for (int it = F.gw; it < NB * 64 * 8; it += F.NGW) {
;     ...
;         for (int g = 0; g < 4; ++g) { unsigned wl[16], wb[16], wg[16];
; #pragma unroll
;             for (int q = 0; q < 16; ++q) { const int t = 63 - (g * 16 + q); wl[q] = __builtin_nontemporal_load(la1 + (size_t)t * (D / 2)); wb[q] = __builtin_nontemporal_load(bb1 + (size_t)t * (D / 2)); wg[q] = __builtin_nontemporal_load(gg + (size_t)t * (D / 2)); }
; #pragma unroll
;             for (int q = 0; q < 16; ++q) { const int t = 63 - (g * 16 + q); hb0 = __expf(bf_lo(wl[q])) * hb0 + bf_lo(wb[q]); hb1 = __expf(bf_hi(wl[q])) * hb1 + bf_hi(wb[q]);
;                 yy[(size_t)t * (D / 2)] = cvt_pk_bf16((fv0[t] + hb0) * bf_lo(wg[q]), (fv1[t] + hb1) * bf_hi(wg[q])); } }
	v_permlane16_swap_b32_e32 v54, v55
	v_permlane16_swap_b32_e32 v56, v57
	v_permlane16_swap_b32_e32 v58, v59
	v_permlane16_swap_b32_e32 v60, v61
	v_permlane16_swap_b32_e32 v62, v63
	v_permlane16_swap_b32_e32 v64, v65
	v_permlane32_swap_b32_e32 v54, v56
	v_permlane32_swap_b32_e32 v55, v57
	v_permlane32_swap_b32_e32 v58, v60
	v_permlane32_swap_b32_e32 v59, v61
	v_permlane32_swap_b32_e32 v62, v64
	v_permlane32_swap_b32_e32 v63, v65
	v_and_b32_e32 v6, 0xffff0000, v54
	v_lshlrev_b32_e32 v54, 16, v54
	v_and_b32_e32 v7, 0xffff0000, v55
	v_lshlrev_b32_e32 v55, 16, v55
	v_and_b32_e32 v14, 0xffff0000, v56
	v_lshlrev_b32_e32 v56, 16, v56
	v_and_b32_e32 v15, 0xffff0000, v57
	v_lshlrev_b32_e32 v57, 16, v57
	v_mul_f32_e32 v54, 0x3fb8aa3b, v54
	v_mul_f32_e32 v6, 0x3fb8aa3b, v6
	v_mul_f32_e32 v55, 0x3fb8aa3b, v55
	v_mul_f32_e32 v7, 0x3fb8aa3b, v7
	v_mul_f32_e32 v56, 0x3fb8aa3b, v56
	v_mul_f32_e32 v14, 0x3fb8aa3b, v14
	v_mul_f32_e32 v57, 0x3fb8aa3b, v57
	v_mul_f32_e32 v15, 0x3fb8aa3b, v15
	v_exp_f32_e32 v54, v54
	v_exp_f32_e32 v6, v6
	v_exp_f32_e32 v55, v55
	v_exp_f32_e32 v7, v7
	v_exp_f32_e32 v56, v56
	v_exp_f32_e32 v14, v14
	v_exp_f32_e32 v57, v57
	v_exp_f32_e32 v15, v15
	v_lshlrev_b32_e32 v12, 16, v61
	v_and_b32_e32 v13, 0xffff0000, v61
	v_fmac_f32_e32 v12, v10, v57
	v_fmac_f32_e32 v13, v11, v15
	v_lshlrev_b32_e32 v17, 16, v65
	v_and_b32_e32 v65, 0xffff0000, v65
	v_add_f32_e32 v74, v74, v12
	v_add_f32_e32 v75, v75, v13
	v_mul_f32_e32 v74, v74, v17
	v_mul_f32_e32 v75, v75, v65
	v_cvt_pk_bf16_f32 v65, v74, v75
	v_lshlrev_b32_e32 v10, 16, v60
	v_and_b32_e32 v11, 0xffff0000, v60
	v_fmac_f32_e32 v10, v12, v56
	v_fmac_f32_e32 v11, v13, v14
	v_lshlrev_b32_e32 v17, 16, v64
	v_and_b32_e32 v64, 0xffff0000, v64
	v_add_f32_e32 v72, v72, v10
	v_add_f32_e32 v73, v73, v11
	v_mul_f32_e32 v72, v72, v17
	v_mul_f32_e32 v73, v73, v64
	v_cvt_pk_bf16_f32 v64, v72, v73
	v_lshlrev_b32_e32 v12, 16, v59
	v_and_b32_e32 v13, 0xffff0000, v59
	v_fmac_f32_e32 v12, v10, v55
	v_fmac_f32_e32 v13, v11, v7
	v_lshlrev_b32_e32 v17, 16, v63
	v_and_b32_e32 v63, 0xffff0000, v63
	v_add_f32_e32 v70, v70, v12
	v_add_f32_e32 v71, v71, v13
	v_mul_f32_e32 v70, v70, v17
	v_mul_f32_e32 v71, v71, v63
	v_cvt_pk_bf16_f32 v63, v70, v71
	v_lshlrev_b32_e32 v10, 16, v58
	v_and_b32_e32 v11, 0xffff0000, v58
	v_fmac_f32_e32 v10, v12, v54
	v_fmac_f32_e32 v11, v13, v6
	v_lshlrev_b32_e32 v17, 16, v62
	v_and_b32_e32 v62, 0xffff0000, v62
	v_add_f32_e32 v68, v68, v10
	v_add_f32_e32 v69, v69, v11
	v_mul_f32_e32 v68, v68, v17
	v_mul_f32_e32 v69, v69, v62
	v_cvt_pk_bf16_f32 v62, v68, v69
	s_nop 1
	v_permlane16_swap_b32_e32 v62, v63
	v_permlane16_swap_b32_e32 v64, v65
	s_nop 1
	v_permlane32_swap_b32_e32 v62, v64
	v_permlane32_swap_b32_e32 v63, v65
	global_store_dwordx4 v5, v[62:65], s[80:81]
	s_add_i32 s1, s1, s2
	s_add_i32 s12, s12, s13
	s_cmpk_gt_i32 s1, 0x7ff
	s_cbranch_scc1 .LBB0_184
